# speedup vs baseline: 1.0128x; 1.0128x over previous
.LBB0_25:
	v_mfma_f32_32x32x16_f16 v[48:63], v[80:83], v[96:99], 0
	v_add_u32_e32 v44, s8, v226
	ds_read_b128 v[32:35], v44
	ds_read_b128 v[36:39], v44 offset:4352
	v_mfma_f32_32x32x16_f16 v[64:79], v[204:207], v[96:99], 0
	s_waitcnt lgkmcnt(1)
	v_mfma_f32_32x32x16_f16 v[48:63], v[88:91], v[32:35], v[48:63]
	ds_read_b128 v[40:43], v44 offset:16
	v_mfma_f32_32x32x16_f16 v[64:79], v[84:87], v[32:35], v[64:79]
	s_waitcnt lgkmcnt(1)
	v_mfma_f32_32x32x16_f16 v[48:63], v[100:103], v[36:39], v[48:63]
	ds_read_b128 v[32:35], v44 offset:4368
	v_mfma_f32_32x32x16_f16 v[64:79], v[92:95], v[36:39], v[64:79]
	s_waitcnt lgkmcnt(1)
	v_mfma_f32_32x32x16_f16 v[48:63], v[108:111], v[40:43], v[48:63]
	ds_read_b128 v[36:39], v44 offset:32
	v_mfma_f32_32x32x16_f16 v[64:79], v[104:107], v[40:43], v[64:79]
	s_waitcnt lgkmcnt(1)
	v_mfma_f32_32x32x16_f16 v[48:63], v[116:119], v[32:35], v[48:63]
	ds_read_b128 v[40:43], v44 offset:4384
	v_mfma_f32_32x32x16_f16 v[64:79], v[112:115], v[32:35], v[64:79]
	s_waitcnt lgkmcnt(1)
	v_mfma_f32_32x32x16_f16 v[48:63], v[120:123], v[36:39], v[48:63]
	ds_read_b128 v[32:35], v44 offset:48
	v_mfma_f32_32x32x16_f16 v[64:79], v[128:131], v[36:39], v[64:79]
	s_waitcnt lgkmcnt(1)
	v_mfma_f32_32x32x16_f16 v[48:63], v[152:155], v[40:43], v[48:63]
	ds_read_b128 v[36:39], v44 offset:4400
	v_mfma_f32_32x32x16_f16 v[64:79], v[124:127], v[40:43], v[64:79]
	s_waitcnt lgkmcnt(1)
	v_mfma_f32_32x32x16_f16 v[48:63], v[136:139], v[32:35], v[48:63]
	ds_read_b128 v[40:43], v44 offset:64
	v_mfma_f32_32x32x16_f16 v[64:79], v[132:135], v[32:35], v[64:79]
	s_waitcnt lgkmcnt(1)
	v_mfma_f32_32x32x16_f16 v[48:63], v[144:147], v[36:39], v[48:63]
	ds_read_b128 v[32:35], v44 offset:4416
	v_mfma_f32_32x32x16_f16 v[64:79], v[140:143], v[36:39], v[64:79]
	s_waitcnt lgkmcnt(1)
	v_mfma_f32_32x32x16_f16 v[48:63], v[156:159], v[40:43], v[48:63]
	ds_read_b128 v[36:39], v44 offset:80
	v_mfma_f32_32x32x16_f16 v[64:79], v[148:151], v[40:43], v[64:79]
	s_waitcnt lgkmcnt(1)
	v_mfma_f32_32x32x16_f16 v[48:63], v[164:167], v[32:35], v[48:63]
	ds_read_b128 v[40:43], v44 offset:4432
	v_mfma_f32_32x32x16_f16 v[64:79], v[160:163], v[32:35], v[64:79]
	s_waitcnt lgkmcnt(1)
	v_mfma_f32_32x32x16_f16 v[48:63], v[172:175], v[36:39], v[48:63]
	ds_read_b128 v[32:35], v44 offset:96
	v_mfma_f32_32x32x16_f16 v[64:79], v[168:171], v[36:39], v[64:79]
	s_waitcnt lgkmcnt(1)
	v_mfma_f32_32x32x16_f16 v[48:63], v[180:183], v[40:43], v[48:63]
	ds_read_b128 v[36:39], v44 offset:4448
	v_mfma_f32_32x32x16_f16 v[64:79], v[176:179], v[40:43], v[64:79]
	s_waitcnt lgkmcnt(1)
	v_mfma_f32_32x32x16_f16 v[48:63], v[188:191], v[32:35], v[48:63]
	v_mfma_f32_32x32x16_f16 v[64:79], v[184:187], v[32:35], v[64:79]
	s_waitcnt lgkmcnt(0)
	v_mfma_f32_32x32x16_f16 v[48:63], v[196:199], v[36:39], v[48:63]
	v_mfma_f32_32x32x16_f16 v[64:79], v[192:195], v[36:39], v[64:79]
	s_cmp_eq_u32 s3, 3
	s_cbranch_scc0 .Lno_pre
	s_cmpk_eq_i32 s8, 0x600
	s_cbranch_scc0 .Lno_pre
	v_mul_u32_u24_e32 v100, 0x4400, v213
	v_add_u32_e32 v100, v100, v210
	v_mov_b32_e32 v101, 0
	v_readfirstlane_b32 s90, v213
	v_lshl_add_u64 v[100:101], v[100:101], 0, s[36:37]
	s_mul_i32 s90, s90, 0x4540
	s_mov_b32 m0, s90
	s_nop 0
	global_load_lds_dwordx4 v[100:101], off
	global_load_lds_dwordx4 v[100:101], off offset:1024
	global_load_lds_dwordx4 v[100:101], off offset:2048
	global_load_lds_dwordx4 v[100:101], off offset:3072
	s_mov_b64 s[92:93], 0x1000
	v_lshl_add_u64 v[102:103], v[100:101], 0, s[92:93]
	s_add_u32 s91, s90, 0x1000
	s_mov_b32 m0, s91
	s_nop 0
	global_load_lds_dwordx4 v[102:103], off
	global_load_lds_dwordx4 v[102:103], off offset:1024
	global_load_lds_dwordx4 v[102:103], off offset:2048
	global_load_lds_dwordx4 v[102:103], off offset:3072
	s_mov_b64 s[92:93], 0x2000
	v_lshl_add_u64 v[102:103], v[100:101], 0, s[92:93]
	s_add_u32 s91, s90, 0x2000
	s_mov_b32 m0, s91
	s_nop 0
	global_load_lds_dwordx4 v[102:103], off
	s_mov_b64 s[92:93], 0x3800
	v_lshl_add_u64 v[102:103], v[100:101], 0, s[92:93]
	s_add_u32 s91, s90, 0x3800
	s_mov_b32 m0, s91
	s_nop 0
	global_load_lds_dwordx4 v[102:103], off
	global_load_lds_dwordx4 v[102:103], off offset:1024
	global_load_lds_dwordx4 v[102:103], off offset:2048
	s_mov_b64 s[92:93], 0x2400
	v_lshl_add_u64 v[102:103], v[100:101], 0, s[92:93]
	global_load_dwordx4 v[104:107], v[102:103], off
	global_load_dwordx4 v[108:111], v[102:103], off offset:1024
	global_load_dwordx4 v[112:115], v[102:103], off offset:2048
	global_load_dwordx4 v[116:119], v[102:103], off offset:3072
	s_mov_b64 s[92:93], 0x3400
	v_lshl_add_u64 v[102:103], v[100:101], 0, s[92:93]
	global_load_dwordx4 v[120:123], v[102:103], off

.LBB0_30:
	v_mov_b32_e32 v209, v245
	v_mul_u32_u24_e32 v101, 0x4540, v213
	v_add_u32_e32 v101, v101, v210
	v_mov_b32_e32 v253, v210
	v_add_u32_e32 v254, 0xcfc0, v210
	v_add_u32_e32 v255, 0x19f80, v210
	s_waitcnt vmcnt(0)
	ds_write_b128 v101, v[104:107] offset:9216
	ds_write_b128 v101, v[108:111] offset:10240
	ds_write_b128 v101, v[112:115] offset:11264
	ds_write_b128 v101, v[116:119] offset:12288
	ds_write_b128 v101, v[120:123] offset:13312
	v_readfirstlane_b32 s0, v213
	s_cmp_lt_i32 s0, 3
	s_waitcnt lgkmcnt(0)
	s_barrier
	s_cbranch_scc0 .LBB0_33
	v_mov_b32_e32 v83, 0
	v_mov_b32_e32 v211, v83
	v_lshl_add_u64 v[156:157], s[36:37], 0, v[210:211]
	s_movk_i32 s0, 0x3000
	v_add_co_u32_e32 v68, vcc, s0, v156
	s_movk_i32 s0, 0x2000
	s_nop 0
	v_addc_co_u32_e32 v69, vcc, 0, v157, vcc
	ds_read_b128 v[0:3], v253 offset:8192
	v_add_co_u32_e32 v70, vcc, s0, v156
	s_movk_i32 s0, 0x1000
	s_nop 0
	v_addc_co_u32_e32 v71, vcc, 0, v157, vcc
	ds_read_b128 v[16:19], v253 offset:9216
	ds_read_b128 v[56:59], v253
	ds_read_b128 v[52:55], v253 offset:1024
	ds_read_b128 v[48:51], v253 offset:2048
	ds_read_b128 v[44:47], v253 offset:3072
	v_add_co_u32_e32 v20, vcc, s0, v156
	s_movk_i32 s0, 0x50
	s_nop 0
	v_addc_co_u32_e32 v21, vcc, 0, v157, vcc
	ds_read_b128 v[40:43], v253 offset:4096
	ds_read_b128 v[36:39], v253 offset:5120
	ds_read_b128 v[32:35], v253 offset:6144
	ds_read_b128 v[60:63], v253 offset:12288
	ds_read_b128 v[72:75], v253 offset:7168
	ds_read_b128 v[76:79], v253 offset:10240
	v_lshl_or_b32 v20, v213, 5, v212
	v_mov_b32_e32 v21, 0x4f
	v_cmp_gt_u32_e64 s[0:1], s0, v20
	s_lshl_b32 s2, s2, 2
	s_movk_i32 s3, 0x4000
	v_cndmask_b32_e64 v100, v21, v20, s[0:1]
	v_lshl_or_b32 v64, v100, 7, v208
	v_add_u32_e32 v127, 0x22a00, v64
	ds_read_b128 v[64:67], v127
	ds_read_b128 v[84:87], v127 offset:32
	s_mov_b32 s9, 0x66666667
	v_add_co_u32_e32 v108, vcc, s3, v156
	s_movk_i32 s10, 0x5000
	s_nop 0
	v_addc_co_u32_e32 v109, vcc, 0, v157, vcc
	v_add_co_u32_e32 v152, vcc, s10, v156
	v_lshlrev_b32_e32 v82, 1, v214
	s_nop 0
	v_addc_co_u32_e32 v153, vcc, 0, v157, vcc
	v_mov_b32_e32 v126, 0x3727c5ac
	s_mov_b32 s8, 0xf800000
	v_mov_b32_e32 v208, 0x260
	v_mov_b32_e32 v80, s26
	v_mov_b32_e32 v81, s27
	s_and_b64 s[0:1], s[4:5], s[0:1]
	s_waitcnt lgkmcnt(12)
	v_mfma_f32_32x32x16_f16 v[16:31], v[16:19], v[96:99], 0
	v_mfma_f32_32x32x16_f16 v[0:15], v[0:3], v[96:99], 0
	s_waitcnt lgkmcnt(1)
	v_mfma_f32_32x32x16_f16 v[0:15], v[56:59], v[64:67], v[0:15]
	s_waitcnt lgkmcnt(1)
	v_mfma_f32_32x32x16_f16 v[16:31], v[52:55], v[64:67], v[16:31]
	v_mul_lo_u16_e32 v52, 0xcd, v100
	v_lshrrev_b16_e32 v52, 10, v52
	v_lshlrev_b32_e32 v102, 10, v52
	v_lshrrev_b32_e32 v101, 2, v52
	v_sub_u32_e32 v103, s2, v52
	s_waitcnt lgkmcnt(0)
	v_mfma_f32_32x32x16_f16 v[0:15], v[48:51], v[84:87], v[0:15]
	ds_read_b128 v[48:51], v127 offset:64
	ds_read_b128 v[88:91], v127 offset:96
	s_waitcnt lgkmcnt(2)
	v_mfma_f32_32x32x16_f16 v[16:31], v[44:47], v[84:87], v[16:31]
	ds_read_b128 v[84:87], v253 offset:18752
	ds_read_b128 v[92:95], v253 offset:19776
	ds_read_b128 v[120:123], v253 offset:11264
	ds_read_b128 v[52:55], v253 offset:13312
	ds_read_b128 v[56:59], v253 offset:14336
	ds_read_b128 v[44:47], v253 offset:15360
	ds_read_b128 v[64:67], v253 offset:16384
	s_waitcnt lgkmcnt(8)
	v_mfma_f32_32x32x16_f16 v[0:15], v[40:43], v[48:51], v[0:15]
	v_and_b32_e32 v40, 0xc00, v102
	v_add3_u32 v40, v103, v101, v40
	v_mad_u64_u32 v[158:159], s[2:3], v40, 5, v[100:101]
	v_mul_hi_i32 v42, v158, s9
	v_lshlrev_b32_e32 v40, 6, v158
	v_ashrrev_i32_e32 v41, 31, v40
	s_waitcnt lgkmcnt(8)
	v_mfma_f32_32x32x16_f16 v[16:31], v[36:39], v[48:51], v[16:31]
	v_lshrrev_b32_e32 v38, 31, v42
	v_ashrrev_i32_e32 v39, 1, v42
	v_add_u32_e32 v159, v39, v38
	v_lshlrev_b32_e32 v68, 6, v159
	v_ashrrev_i32_e32 v69, 31, v68
	v_lshl_add_u64 v[48:49], v[68:69], 2, s[24:25]
	v_lshl_add_u64 v[36:37], v[40:41], 1, s[6:7]
	s_waitcnt lgkmcnt(7)
	v_mfma_f32_32x32x16_f16 v[0:15], v[32:35], v[88:91], v[0:15]
	v_lshl_add_u64 v[70:71], v[36:37], 0, v[82:83]
	v_lshlrev_b32_e32 v82, 2, v216
	v_lshl_add_u64 v[116:117], v[48:49], 0, v[82:83]
	global_load_dwordx4 v[32:35], v82, s[28:29]
	global_load_dwordx4 v[36:39], v82, s[28:29] offset:32
	global_load_dwordx4 v[40:43], v82, s[28:29] offset:64
	global_load_dwordx4 v[128:131], v82, s[28:29] offset:96
	v_add_u32_e32 v68, 0x40000, v68
	s_mov_b32 s6, 0xd000
	s_mov_b32 s7, 0xc000
	s_waitcnt lgkmcnt(7)
	v_mfma_f32_32x32x16_f16 v[16:31], v[72:75], v[88:91], v[16:31]
	s_nop 11
	v_add_f32_e32 v69, v0, v16
	v_add_f32_e32 v90, v1, v17
	v_add_f32_e32 v69, 0, v69
	v_add_f32_e32 v91, v2, v18
	v_add_f32_e32 v69, v90, v69
	v_add_f32_e32 v100, v3, v19
	v_add_f32_e32 v69, v91, v69
	v_add_f32_e32 v101, v4, v20
	v_add_f32_e32 v69, v100, v69
	v_add_f32_e32 v102, v5, v21
	v_add_f32_e32 v69, v101, v69
	v_pk_add_f32 v[48:49], v[6:7], v[22:23]
	v_add_f32_e32 v69, v102, v69
	v_add_f32_e32 v48, v48, v69
	v_pk_add_f32 v[50:51], v[8:9], v[24:25]
	v_add_f32_e32 v48, v49, v48
	v_add_f32_e32 v48, v50, v48
	v_pk_add_f32 v[72:73], v[10:11], v[26:27]
	v_add_f32_e32 v48, v51, v48
	v_add_f32_e32 v48, v72, v48
	v_pk_add_f32 v[74:75], v[12:13], v[28:29]
	v_add_f32_e32 v48, v73, v48
	v_add_f32_e32 v48, v74, v48
	v_pk_add_f32 v[88:89], v[14:15], v[30:31]
	v_add_f32_e32 v48, v75, v48
	v_add_f32_e32 v48, v88, v48
	v_add_f32_e32 v69, v89, v48
	ds_bpermute_b32 v72, v209, v69
	global_load_dwordx4 v[48:51], v[116:117], off
	global_load_dwordx4 v[88:91], v[116:117], off offset:32
	global_load_dwordx4 v[132:135], v[116:117], off offset:64
	global_load_dwordx4 v[136:139], v[116:117], off offset:96
	global_load_dwordx4 v[104:107], v[70:71], off
	global_load_dwordx4 v[100:103], v[70:71], off offset:32
	global_load_dwordx4 v[140:143], v82, s[28:29] offset:128
	global_load_dwordx4 v[144:147], v82, s[28:29] offset:160
	global_load_dwordx4 v[148:151], v[116:117], off offset:128
	global_load_dwordx4 v[160:163], v82, s[28:29] offset:192
	global_load_dwordx4 v[164:167], v[116:117], off offset:160
	global_load_dwordx4 v[168:171], v[116:117], off offset:192
	ds_read_b128 v[172:175], v253 offset:17728
	s_waitcnt lgkmcnt(1)
	v_add_f32_e32 v69, v69, v72
	v_mul_f32_e32 v72, 0x3c800000, v69
	v_pk_add_f32 v[124:125], v[30:31], v[72:73] op_sel_hi:[1,0] neg_lo:[0,1] neg_hi:[0,1]
	v_pk_add_f32 v[154:155], v[14:15], v[72:73] op_sel_hi:[1,0] neg_lo:[0,1] neg_hi:[0,1]
	v_pk_add_f32 v[184:185], v[28:29], v[72:73] op_sel_hi:[1,0] neg_lo:[0,1] neg_hi:[0,1]
	v_pk_add_f32 v[186:187], v[12:13], v[72:73] op_sel_hi:[1,0] neg_lo:[0,1] neg_hi:[0,1]
	v_pk_add_f32 v[188:189], v[26:27], v[72:73] op_sel_hi:[1,0] neg_lo:[0,1] neg_hi:[0,1]
	v_pk_add_f32 v[190:191], v[10:11], v[72:73] op_sel_hi:[1,0] neg_lo:[0,1] neg_hi:[0,1]
	v_pk_add_f32 v[192:193], v[24:25], v[72:73] op_sel_hi:[1,0] neg_lo:[0,1] neg_hi:[0,1]
	v_pk_add_f32 v[194:195], v[8:9], v[72:73] op_sel_hi:[1,0] neg_lo:[0,1] neg_hi:[0,1]
	v_pk_add_f32 v[196:197], v[22:23], v[72:73] op_sel_hi:[1,0] neg_lo:[0,1] neg_hi:[0,1]
	v_pk_add_f32 v[74:75], v[6:7], v[72:73] op_sel_hi:[1,0] neg_lo:[0,1] neg_hi:[0,1]
	v_pk_add_f32 v[198:199], v[20:21], v[72:73] op_sel_hi:[1,0] neg_lo:[0,1] neg_hi:[0,1]
	v_pk_add_f32 v[118:119], v[4:5], v[72:73] op_sel_hi:[1,0] neg_lo:[0,1] neg_hi:[0,1]
	v_pk_add_f32 v[200:201], v[18:19], v[72:73] op_sel_hi:[1,0] neg_lo:[0,1] neg_hi:[0,1]
	v_pk_add_f32 v[202:203], v[2:3], v[72:73] op_sel_hi:[1,0] neg_lo:[0,1] neg_hi:[0,1]
	v_pk_add_f32 v[204:205], v[16:17], v[72:73] op_sel_hi:[1,0] neg_lo:[0,1] neg_hi:[0,1]
	v_pk_add_f32 v[72:73], v[0:1], v[72:73] op_sel_hi:[1,0] neg_lo:[0,1] neg_hi:[0,1]
	global_load_dwordx4 v[112:115], v[70:71], off offset:64
	global_load_dwordx4 v[108:111], v[70:71], off offset:96
	global_load_dwordx4 v[176:179], v82, s[28:29] offset:224
	global_load_dwordx4 v[180:183], v[116:117], off offset:224
	v_fma_f32 v0, v72, v72, 0
	v_fmac_f32_e32 v0, v204, v204
	v_fmac_f32_e32 v0, v73, v73
	v_fmac_f32_e32 v0, v205, v205
	v_fmac_f32_e32 v0, v202, v202
	v_fmac_f32_e32 v0, v200, v200
	v_fmac_f32_e32 v0, v203, v203
	v_fmac_f32_e32 v0, v201, v201
	v_fmac_f32_e32 v0, v118, v118
	v_fmac_f32_e32 v0, v198, v198
	v_fmac_f32_e32 v0, v119, v119
	v_fmac_f32_e32 v0, v199, v199
	v_fmac_f32_e32 v0, v74, v74
	v_fmac_f32_e32 v0, v196, v196
	v_fmac_f32_e32 v0, v75, v75
	v_fmac_f32_e32 v0, v197, v197
	v_fmac_f32_e32 v0, v194, v194
	v_fmac_f32_e32 v0, v192, v192
	v_fmac_f32_e32 v0, v195, v195
	v_fmac_f32_e32 v0, v193, v193
	v_fmac_f32_e32 v0, v190, v190
	v_fmac_f32_e32 v0, v188, v188
	v_fmac_f32_e32 v0, v191, v191
	v_fmac_f32_e32 v0, v189, v189
	v_fmac_f32_e32 v0, v186, v186
	v_fmac_f32_e32 v0, v184, v184
	v_fmac_f32_e32 v0, v187, v187
	v_fmac_f32_e32 v0, v185, v185
	v_fmac_f32_e32 v0, v154, v154
	v_fmac_f32_e32 v0, v124, v124
	v_fmac_f32_e32 v0, v155, v155
	v_fmac_f32_e32 v0, v125, v125
	ds_bpermute_b32 v1, v209, v0
	s_waitcnt lgkmcnt(0)
	v_add_f32_e32 v0, v0, v1
	v_fmamk_f32 v0, v0, 0x3c800000, v126
	v_mul_f32_e32 v1, 0x4f800000, v0
	v_cmp_gt_f32_e32 vcc, s8, v0
	s_nop 1
	v_cndmask_b32_e32 v0, v0, v1, vcc
	v_sqrt_f32_e32 v1, v0
	s_nop 0
	v_add_u32_e32 v2, -1, v1
	v_fma_f32 v3, -v2, v1, v0
	v_cmp_ge_f32_e64 s[2:3], 0, v3
	v_add_u32_e32 v3, 1, v1
	s_nop 0
	v_cndmask_b32_e64 v2, v1, v2, s[2:3]
	v_fma_f32 v1, -v3, v1, v0
	v_cmp_lt_f32_e64 s[2:3], 0, v1
	s_nop 1
	v_cndmask_b32_e64 v1, v2, v3, s[2:3]
	v_mul_f32_e32 v2, 0x37800000, v1
	v_cndmask_b32_e32 v1, v1, v2, vcc
	v_cmp_class_f32_e32 vcc, v0, v208
	s_nop 1
	v_cndmask_b32_e32 v69, v1, v0, vcc
	v_div_scale_f32 v16, s[2:3], v69, v69, 1.0
	v_rcp_f32_e32 v206, v16
	s_waitcnt lgkmcnt(0)
	v_mfma_f32_32x32x16_f16 v[0:15], v[84:87], v[96:99], 0
	ds_read_b128 v[84:87], v127 offset:10240
	s_mov_b32 s2, 0xa000
	v_fma_f32 v17, -v16, v206, 1.0
	v_fmac_f32_e32 v206, v17, v206
	v_div_scale_f32 v17, vcc, 1.0, v69, 1.0
	v_mul_f32_e32 v70, v17, v206
	v_fma_f32 v18, -v16, v70, v17
	v_fmac_f32_e32 v70, v18, v206
	v_fma_f32 v71, -v16, v70, v17
	s_waitcnt lgkmcnt(1)
	v_mfma_f32_32x32x16_f16 v[16:31], v[92:95], v[96:99], 0
	ds_read_b128 v[92:95], v127 offset:10272
	v_div_fmas_f32 v70, v71, v206, v70
	v_div_fixup_f32 v70, v70, v69, 1.0
	v_mul_f32_e64 v210, v118, v70
	v_mul_f32_e64 v211, v119, v70
	v_pk_mul_f32 v[206:207], v[74:75], v[70:71] op_sel_hi:[1,0]
	v_pk_mul_f32 v[74:75], v[202:203], v[70:71] op_sel_hi:[1,0]
	s_waitcnt vmcnt(14) lgkmcnt(2)
	v_pk_fma_f32 v[36:37], v[210:211], v[36:37], v[88:89]
	s_waitcnt vmcnt(14) lgkmcnt(1)
	v_mfma_f32_32x32x16_f16 v[0:15], v[76:79], v[84:87], v[0:15]
	v_fma_f32 v34, v74, v34, v50
	v_fma_f32 v35, v75, v35, v51
	v_fma_f32 v38, v206, v38, v90
	v_fma_f32 v39, v207, v39, v91
	v_cvt_pk_f16_f32 v50, v36, v37
	v_pk_mul_f32 v[36:37], v[154:155], v[70:71] op_sel_hi:[1,0]
	v_cvt_pk_f16_f32 v51, v38, v39
	v_pk_mul_f32 v[38:39], v[186:187], v[70:71] op_sel_hi:[1,0]
	s_waitcnt vmcnt(12) lgkmcnt(1)
	v_pk_fma_f32 v[36:37], v[36:37], v[130:131], v[138:139]
	v_mfma_f32_32x32x16_f16 v[16:31], v[120:123], v[84:87], v[16:31]
	ds_read_b128 v[84:87], v127 offset:10336
	v_mul_f32_e64 v72, v72, v70
	v_mul_f32_e64 v73, v73, v70
	v_mul_f32_e64 v88, v184, v70
	v_mul_f32_e64 v89, v185, v70
	v_pk_fma_f32 v[32:33], v[72:73], v[32:33], v[48:49]
	v_cvt_pk_f16_f32 v49, v34, v35
	v_cvt_pk_f16_f32 v48, v32, v33
	v_pk_mul_f32 v[32:33], v[190:191], v[70:71] op_sel_hi:[1,0]
	s_waitcnt vmcnt(12) lgkmcnt(1)
	v_mfma_f32_32x32x16_f16 v[0:15], v[60:63], v[92:95], v[0:15]
	v_fma_f32 v60, v38, v128, v136
	v_fma_f32 v61, v39, v129, v137
	v_mul_f32_e64 v62, v204, v70
	v_mul_f32_e64 v63, v205, v70
	v_mul_f32_e64 v34, v194, v70
	v_mul_f32_e64 v35, v195, v70
	s_waitcnt vmcnt(7) lgkmcnt(1)
	v_pk_fma_f32 v[62:63], v[62:63], v[140:141], v[148:149]
	v_pk_fma_f32 v[40:41], v[34:35], v[40:41], v[132:133]
	v_pk_fma_f32 v[42:43], v[32:33], v[42:43], v[134:135]
	global_load_dwordx4 v[116:119], v82, s[30:31]
	global_load_dwordx4 v[72:75], v82, s[30:31] offset:32
	v_mfma_f32_32x32x16_f16 v[16:31], v[52:55], v[92:95], v[16:31]
	v_cvt_pk_f16_f32 v55, v36, v37
	ds_read_b128 v[36:39], v127 offset:10304
	v_cvt_pk_f16_f32 v54, v60, v61
	v_mul_f32_e64 v60, v200, v70
	v_mul_f32_e64 v61, v201, v70
	global_load_dwordx4 v[76:79], v82, s[30:31] offset:64
	global_load_dwordx4 v[32:35], v82, s[30:31] offset:96
	v_pk_fma_f32 v[60:61], v[60:61], v[142:143], v[150:151]
	s_waitcnt vmcnt(11) lgkmcnt(0)
	v_mfma_f32_32x32x16_f16 v[0:15], v[56:59], v[36:39], v[0:15]
	v_mul_f32_e64 v56, v196, v70
	v_mul_f32_e64 v57, v197, v70
	v_mul_f32_e64 v58, v198, v70
	v_mul_f32_e64 v59, v199, v70
	v_cvt_pk_f16_f32 v53, v42, v43
	v_cvt_pk_f16_f32 v52, v40, v41
	global_load_dwordx4 v[40:43], v82, s[30:31] offset:128
	v_mfma_f32_32x32x16_f16 v[16:31], v[44:47], v[36:39], v[16:31]
	s_waitcnt vmcnt(10) lgkmcnt(0)
	v_fma_f32 v38, v56, v146, v166
	v_fma_f32 v39, v57, v147, v167
	v_cvt_pk_f16_f32 v57, v60, v61
	v_mul_f32_e64 v60, v188, v70
	v_mul_f32_e64 v61, v189, v70
	v_cvt_pk_f16_f32 v56, v62, v63
	v_pk_mul_f32 v[62:63], v[124:125], v[70:71] op_sel_hi:[1,0]
	s_waitcnt vmcnt(9) lgkmcnt(0)
	v_pk_fma_f32 v[60:61], v[60:61], v[162:163], v[170:171]
	v_add_co_u32_e32 v170, vcc, s2, v156
	v_mfma_f32_32x32x16_f16 v[0:15], v[64:67], v[84:87], v[0:15]
	v_mul_f32_e64 v64, v192, v70
	v_mul_f32_e64 v65, v193, v70
	v_fma_f32 v36, v58, v144, v164
	v_fma_f32 v37, v59, v145, v165
	v_fma_f32 v136, v64, v160, v168
	v_fma_f32 v137, v65, v161, v169
	s_waitcnt vmcnt(5) lgkmcnt(0)
	v_pk_fma_f32 v[70:71], v[88:89], v[176:177], v[180:181]
	v_pk_fma_f32 v[62:63], v[62:63], v[178:179], v[182:183]
	v_addc_co_u32_e32 v171, vcc, 0, v157, vcc
	v_mfma_f32_32x32x16_f16 v[16:31], v[172:175], v[84:87], v[16:31]
	global_load_dwordx4 v[44:47], v82, s[30:31] offset:160
	v_cvt_pk_f16_f32 v59, v38, v39
	v_cvt_pk_f16_f32 v58, v36, v37
	global_load_dwordx4 v[36:39], v82, s[30:31] offset:192
	v_cvt_pk_f16_f32 v63, v62, v63
	v_cvt_pk_f16_f32 v62, v70, v71
	s_movk_i32 s2, 0x7000
	s_nop 4
	v_add_f32_e32 v64, v0, v16
	v_add_f32_e32 v64, 0, v64
	v_add_f32_e32 v65, v1, v17
	v_add_f32_e32 v64, v65, v64
	v_add_f32_e32 v65, v2, v18
	v_add_f32_e32 v64, v65, v64
	v_add_f32_e32 v65, v3, v19
	v_add_f32_e32 v64, v65, v64
	v_add_f32_e32 v65, v4, v20
	v_add_f32_e32 v64, v65, v64
	v_add_f32_e32 v65, v5, v21
	v_add_f32_e32 v66, v65, v64
	v_pk_add_f32 v[64:65], v[6:7], v[22:23]
	v_add_co_u32_e32 v184, vcc, s2, v156
	v_add_f32_e32 v64, v64, v66
	v_add_f32_e32 v66, v65, v64
	v_pk_add_f32 v[64:65], v[8:9], v[24:25]
	v_addc_co_u32_e32 v185, vcc, 0, v157, vcc
	v_add_f32_e32 v64, v64, v66
	v_add_f32_e32 v66, v65, v64
	v_pk_add_f32 v[64:65], v[10:11], v[26:27]
	s_movk_i32 s2, 0x6000
	v_add_f32_e32 v64, v64, v66
	v_add_f32_e32 v66, v65, v64
	v_pk_add_f32 v[64:65], v[12:13], v[28:29]
	v_add_co_u32_e32 v186, vcc, s2, v156
	v_add_f32_e32 v64, v64, v66
	v_add_f32_e32 v66, v65, v64
	v_pk_add_f32 v[64:65], v[14:15], v[30:31]
	v_addc_co_u32_e32 v187, vcc, 0, v157, vcc
	v_add_f32_e32 v64, v64, v66
	v_add_f32_e32 v69, v65, v64
	ds_bpermute_b32 v84, v209, v69
	global_load_dwordx4 v[64:67], v82, s[30:31] offset:224
	v_cvt_pk_f16_f32 v61, v60, v61
	v_cvt_pk_f16_f32 v60, v136, v137
	s_waitcnt vmcnt(8) lgkmcnt(0)
	v_add_f32_e32 v69, v69, v84
	v_mul_f32_e32 v92, 0x3c800000, v69
	v_ashrrev_i32_e32 v69, 31, v68
	v_lshl_add_u64 v[68:69], v[68:69], 2, s[24:25]
	v_lshl_add_u64 v[124:125], v[68:69], 0, v[82:83]
	global_load_dwordx4 v[140:143], v[124:125], off
	global_load_dwordx4 v[88:91], v[124:125], off offset:32
	global_load_dwordx4 v[84:87], v[124:125], off offset:64
	global_load_dwordx4 v[68:71], v[124:125], off offset:96
	v_pk_add_f32 v[180:181], v[10:11], v[92:93] op_sel_hi:[1,0] neg_lo:[0,1] neg_hi:[0,1]
	v_pk_add_f32 v[182:183], v[8:9], v[92:93] op_sel_hi:[1,0] neg_lo:[0,1] neg_hi:[0,1]
	v_pk_add_f32 v[8:9], v[2:3], v[92:93] op_sel_hi:[1,0] neg_lo:[0,1] neg_hi:[0,1]
	v_pk_add_f32 v[10:11], v[0:1], v[92:93] op_sel_hi:[1,0] neg_lo:[0,1] neg_hi:[0,1]
	ds_read_b128 v[0:3], v253 offset:37504
	v_pk_add_f32 v[178:179], v[12:13], v[92:93] op_sel_hi:[1,0] neg_lo:[0,1] neg_hi:[0,1]
	v_pk_add_f32 v[174:175], v[16:17], v[92:93] op_sel_hi:[1,0] neg_lo:[0,1] neg_hi:[0,1]
	v_fma_f32 v12, v10, v10, 0
	v_fmac_f32_e32 v12, v174, v174
	v_fmac_f32_e32 v12, v11, v11
	v_fmac_f32_e32 v12, v175, v175
	v_pk_add_f32 v[172:173], v[18:19], v[92:93] op_sel_hi:[1,0] neg_lo:[0,1] neg_hi:[0,1]
	v_fmac_f32_e32 v12, v8, v8
	ds_read_b128 v[144:147], v253 offset:20800
	ds_read_b128 v[148:151], v253 offset:22848
	v_fmac_f32_e32 v12, v172, v172
	v_fmac_f32_e32 v12, v9, v9
	v_pk_add_f32 v[4:5], v[4:5], v[92:93] op_sel_hi:[1,0] neg_lo:[0,1] neg_hi:[0,1]
	v_fmac_f32_e32 v12, v173, v173
	v_pk_add_f32 v[168:169], v[20:21], v[92:93] op_sel_hi:[1,0] neg_lo:[0,1] neg_hi:[0,1]
	v_fmac_f32_e32 v12, v4, v4
	v_fmac_f32_e32 v12, v168, v168
	v_fmac_f32_e32 v12, v5, v5
	v_pk_add_f32 v[6:7], v[6:7], v[92:93] op_sel_hi:[1,0] neg_lo:[0,1] neg_hi:[0,1]
	v_fmac_f32_e32 v12, v169, v169
	v_pk_add_f32 v[166:167], v[22:23], v[92:93] op_sel_hi:[1,0] neg_lo:[0,1] neg_hi:[0,1]
	v_fmac_f32_e32 v12, v6, v6
	v_fmac_f32_e32 v12, v166, v166
	v_fmac_f32_e32 v12, v7, v7
	v_fmac_f32_e32 v12, v167, v167
	v_pk_add_f32 v[164:165], v[24:25], v[92:93] op_sel_hi:[1,0] neg_lo:[0,1] neg_hi:[0,1]
	v_fmac_f32_e32 v12, v182, v182
	v_fmac_f32_e32 v12, v164, v164
	v_fmac_f32_e32 v12, v183, v183
	v_fmac_f32_e32 v12, v165, v165
	v_pk_add_f32 v[162:163], v[26:27], v[92:93] op_sel_hi:[1,0] neg_lo:[0,1] neg_hi:[0,1]
	v_fmac_f32_e32 v12, v180, v180
	v_fmac_f32_e32 v12, v162, v162
	v_fmac_f32_e32 v12, v181, v181
	v_fmac_f32_e32 v12, v163, v163
	v_pk_add_f32 v[160:161], v[28:29], v[92:93] op_sel_hi:[1,0] neg_lo:[0,1] neg_hi:[0,1]
	v_fmac_f32_e32 v12, v178, v178
	v_fmac_f32_e32 v12, v160, v160
	v_pk_add_f32 v[154:155], v[30:31], v[92:93] op_sel_hi:[1,0] neg_lo:[0,1] neg_hi:[0,1]
	v_pk_add_f32 v[176:177], v[14:15], v[92:93] op_sel_hi:[1,0] neg_lo:[0,1] neg_hi:[0,1]
	v_fmac_f32_e32 v12, v179, v179
	ds_read_b128 v[92:95], v253 offset:24896
	global_load_dwordx4 v[28:31], v[124:125], off offset:128
	global_load_dwordx4 v[20:23], v[124:125], off offset:160
	v_fmac_f32_e32 v12, v161, v161
	v_fmac_f32_e32 v12, v176, v176
	ds_read_b128 v[120:123], v253 offset:26944
	v_fmac_f32_e32 v12, v154, v154
	v_fmac_f32_e32 v12, v177, v177
	v_fmac_f32_e32 v12, v155, v155
	ds_bpermute_b32 v13, v209, v12
	s_waitcnt vmcnt(14) lgkmcnt(0)
	v_add_f32_e32 v12, v12, v13
	v_fmac_f32_e32 v126, 0x3c800000, v12
	v_mul_f32_e32 v12, 0x4f800000, v126
	v_cmp_gt_f32_e32 vcc, s8, v126
	s_nop 1
	v_cndmask_b32_e32 v12, v126, v12, vcc
	global_load_dwordx4 v[24:27], v[124:125], off offset:192
	global_load_dwordx4 v[16:19], v[124:125], off offset:224
	s_nop 0
	ds_read_b128 v[124:127], v253 offset:28992
	ds_read_b128 v[128:131], v253 offset:31040
	v_sqrt_f32_e32 v13, v12
	s_nop 0
	v_add_u32_e32 v14, -1, v13
	v_fma_f32 v15, -v14, v13, v12
	v_cmp_ge_f32_e64 s[2:3], 0, v15
	v_add_u32_e32 v15, 1, v13
	s_nop 0
	v_cndmask_b32_e64 v14, v13, v14, s[2:3]
	v_fma_f32 v13, -v15, v13, v12
	v_cmp_lt_f32_e64 s[2:3], 0, v13
	s_nop 1
	v_cndmask_b32_e64 v13, v14, v15, s[2:3]
	v_mul_f32_e32 v14, 0x37800000, v13
	s_mov_b32 s2, 0x8000
	v_cndmask_b32_e32 v13, v13, v14, vcc
	v_add_co_u32_e32 v188, vcc, s2, v156
	s_nop 1
	v_addc_co_u32_e32 v189, vcc, 0, v157, vcc
	v_cmp_class_f32_e32 vcc, v12, v208
	ds_read_b128 v[132:135], v253 offset:33088
	ds_read_b128 v[136:139], v253 offset:35456
	v_cndmask_b32_e32 v12, v13, v12, vcc
	v_div_scale_f32 v13, s[2:3], v12, v12, 1.0
	v_rcp_f32_e32 v14, v13
	s_mov_b32 s2, 0x9000
	s_mov_b32 s3, 0xbc90
	v_fma_f32 v15, -v13, v14, 1.0
	v_fmac_f32_e32 v14, v15, v14
	v_div_scale_f32 v15, vcc, 1.0, v12, 1.0
	v_mul_f32_e32 v82, v15, v14
	v_fma_f32 v190, -v13, v82, v15
	v_fmac_f32_e32 v82, v190, v14
	v_fma_f32 v13, -v13, v82, v15
	v_div_fmas_f32 v13, v13, v14, v82
	v_div_fixup_f32 v82, v13, v12, 1.0
	v_pk_mul_f32 v[190:191], v[6:7], v[82:83] op_sel_hi:[1,0]
	v_pk_mul_f32 v[192:193], v[4:5], v[82:83] op_sel_hi:[1,0]
	v_pk_mul_f32 v[4:5], v[8:9], v[82:83] op_sel_hi:[1,0]
	v_pk_mul_f32 v[6:7], v[10:11], v[82:83] op_sel_hi:[1,0]
	s_waitcnt vmcnt(7) lgkmcnt(4)
	v_pk_fma_f32 v[118:119], v[4:5], v[118:119], v[142:143]
	v_pk_fma_f32 v[116:117], v[6:7], v[116:117], v[140:141]
	s_waitcnt vmcnt(4) lgkmcnt(4)
	v_mfma_f32_32x32x16_f16 v[0:15], v[0:3], v[96:99], 0
	v_fma_f32 v72, v192, v72, v88
	v_fma_f32 v73, v193, v73, v89
	v_fma_f32 v74, v190, v74, v90
	v_fma_f32 v75, v191, v75, v91
	ds_read_b128 v[88:91], v253 offset:21824
	v_cvt_pk_f16_f32 v75, v74, v75
	v_cvt_pk_f16_f32 v74, v72, v73
	v_cvt_pk_f16_f32 v73, v118, v119
	v_pk_mul_f32 v[118:119], v[178:179], v[82:83] op_sel_hi:[1,0]
	s_waitcnt vmcnt(4) lgkmcnt(5)
	v_mfma_f32_32x32x16_f16 v[0:15], v[144:147], v[104:107], v[0:15]
	v_mul_f32_e64 v144, v180, v82
	v_mul_f32_e64 v145, v181, v82
	v_mul_f32_e64 v146, v182, v82
	v_mul_f32_e64 v147, v183, v82
	v_fma_f32 v144, v144, v78, v86
	v_fma_f32 v145, v145, v79, v87
	v_pk_fma_f32 v[146:147], v[146:147], v[76:77], v[84:85]
	ds_read_b128 v[84:87], v253 offset:23872
	v_add_co_u32_e32 v152, vcc, s2, v156
	s_waitcnt vmcnt(4) lgkmcnt(6)
	v_mfma_f32_32x32x16_f16 v[0:15], v[148:151], v[100:103], v[0:15]
	v_addc_co_u32_e32 v153, vcc, 0, v157, vcc
	v_fma_f32 v32, v118, v32, v68
	v_fma_f32 v33, v119, v33, v69
	v_cvt_pk_f16_f32 v69, v144, v145
	v_cvt_pk_f16_f32 v68, v146, v147
	ds_read_b128 v[144:147], v253 offset:27968
	ds_read_b128 v[148:151], v253 offset:32064
	s_waitcnt vmcnt(4) lgkmcnt(8)
	v_mfma_f32_32x32x16_f16 v[0:15], v[92:95], v[112:115], v[0:15]
	ds_read_b128 v[92:95], v253 offset:38528
	ds_read_b128 v[76:79], v253 offset:44672
	v_cvt_pk_f16_f32 v72, v116, v117
	v_mul_f32_e64 v116, v176, v82
	v_mul_f32_e64 v117, v177, v82
	v_pk_mul_f32 v[118:119], v[174:175], v[82:83] op_sel_hi:[1,0]
	v_pk_fma_f32 v[34:35], v[116:117], v[34:35], v[70:71]
	v_pk_mul_f32 v[116:117], v[172:173], v[82:83] op_sel_hi:[1,0]
	s_waitcnt vmcnt(2) lgkmcnt(10)
	v_mfma_f32_32x32x16_f16 v[0:15], v[120:123], v[108:111], v[0:15]
	ds_read_b128 v[120:123], v253 offset:30016
	v_fma_f32 v28, v118, v40, v28
	v_fma_f32 v29, v119, v41, v29
	v_fma_f32 v30, v116, v42, v30
	v_fma_f32 v31, v117, v43, v31
	v_cvt_pk_f16_f32 v40, v28, v29
	v_cvt_pk_f16_f32 v41, v30, v31
	v_pk_mul_f32 v[28:29], v[162:163], v[82:83] op_sel_hi:[1,0]
	v_pk_mul_f32 v[30:31], v[164:165], v[82:83] op_sel_hi:[1,0]
	s_waitcnt vmcnt(0) lgkmcnt(10)
	v_mfma_f32_32x32x16_f16 v[0:15], v[124:127], v[48:51], v[0:15]
	v_fma_f32 v24, v30, v36, v24
	v_fma_f32 v25, v31, v37, v25
	v_fma_f32 v26, v28, v38, v26
	v_fma_f32 v27, v29, v39, v27
	ds_read_b128 v[36:39], v253 offset:34112
	v_cvt_pk_f16_f32 v71, v34, v35
	v_cvt_pk_f16_f32 v70, v32, v33
	v_pk_mul_f32 v[32:33], v[166:167], v[82:83] op_sel_hi:[1,0]
	v_pk_mul_f32 v[34:35], v[168:169], v[82:83] op_sel_hi:[1,0]
	s_waitcnt vmcnt(0) lgkmcnt(10)
	v_mfma_f32_32x32x16_f16 v[0:15], v[128:131], v[52:55], v[0:15]
	ds_read_b128 v[126:129], v253 offset:25920
	v_fma_f32 v20, v34, v44, v20
	v_fma_f32 v21, v35, v45, v21
	v_fma_f32 v22, v32, v46, v22
	v_fma_f32 v23, v33, v47, v23
	v_cvt_pk_f16_f32 v42, v20, v21
	v_cvt_pk_f16_f32 v43, v22, v23
	v_pk_mul_f32 v[20:21], v[154:155], v[82:83] op_sel_hi:[1,0]
	v_pk_mul_f32 v[22:23], v[160:161], v[82:83] op_sel_hi:[1,0]
	s_waitcnt vmcnt(0) lgkmcnt(10)
	v_mfma_f32_32x32x16_f16 v[0:15], v[132:135], v[56:59], v[0:15]
	v_fma_f32 v16, v22, v64, v16
	v_fma_f32 v17, v23, v65, v17
	v_fma_f32 v18, v20, v66, v18
	v_fma_f32 v19, v21, v67, v19
	ds_read_b128 v[64:67], v253 offset:36480
	s_mov_b32 s2, 0xa714
	v_mov_b32_e32 v164, 0xb7d0
	v_cvt_pk_f16_f32 v34, v16, v17
	v_cvt_pk_f16_f32 v35, v18, v19
	s_waitcnt vmcnt(0) lgkmcnt(10)
	v_mfma_f32_32x32x16_f16 v[0:15], v[136:139], v[60:63], v[0:15]
	v_cvt_pk_f16_f32 v33, v26, v27
	v_cvt_pk_f16_f32 v32, v24, v25
	ds_read_b128 v[132:135], v253 offset:39552
	v_add_co_u32_e32 v136, vcc, s6, v156
	ds_read_b128 v[140:143], v253 offset:41600
	ds_read_b128 v[44:47], v253 offset:40576
	s_nop 5
	v_cvt_pk_f16_f32 v0, v0, v1
	v_and_b32_e32 v1, 0x7fff7fff, v0
	v_cvt_pk_f16_f32 v2, v2, v3
	v_pk_fma_f16 v16, v1, s2, v164 op_sel_hi:[1,0,0]
	v_and_b32_e32 v3, 0x7fff7fff, v2
	v_pk_fma_f16 v16, v16, v1, s3 op_sel_hi:[1,1,0]
	v_pk_fma_f16 v18, v3, s2, v164 op_sel_hi:[1,0,0]
	v_pk_mul_f16 v16, v1, v16
	v_pk_fma_f16 v18, v18, v3, s3 op_sel_hi:[1,1,0]
	v_exp_f16_e32 v17, v16
	v_exp_f16_sdwa v16, v16 dst_sel:DWORD dst_unused:UNUSED_PAD src0_sel:WORD_1
	v_pk_mul_f16 v18, v3, v18
	v_pk_add_f16 v0, v1, v0
	v_exp_f16_e32 v19, v18
	v_exp_f16_sdwa v18, v18 dst_sel:DWORD dst_unused:UNUSED_PAD src0_sel:WORD_1
	v_pack_b32_f16 v16, v17, v16
	v_pk_fma_f16 v116, v1, v16, v0 neg_lo:[1,0,0] neg_hi:[1,0,0]
	v_pk_add_f16 v1, v3, v2
	v_pack_b32_f16 v0, v19, v18
	v_pk_fma_f16 v117, v3, v0, v1 neg_lo:[1,0,0] neg_hi:[1,0,0]
	v_cvt_pk_f16_f32 v0, v4, v5
	v_and_b32_e32 v1, 0x7fff7fff, v0
	v_pk_fma_f16 v2, v1, s2, v164 op_sel_hi:[1,0,0]
	s_waitcnt vmcnt(0) lgkmcnt(8)
	v_mfma_f32_32x32x16_f16 v[16:31], v[92:95], v[96:99], 0
	v_pk_fma_f16 v2, v2, v1, s3 op_sel_hi:[1,1,0]
	v_cvt_pk_f16_f32 v4, v6, v7
	v_pk_mul_f16 v2, v1, v2
	v_and_b32_e32 v5, 0x7fff7fff, v4
	v_exp_f16_e32 v3, v2
	v_exp_f16_sdwa v2, v2 dst_sel:DWORD dst_unused:UNUSED_PAD src0_sel:WORD_1
	v_pk_fma_f16 v6, v5, s2, v164 op_sel_hi:[1,0,0]
	v_pk_add_f16 v0, v1, v0
	v_pk_fma_f16 v6, v6, v5, s3 op_sel_hi:[1,1,0]
	v_pack_b32_f16 v2, v3, v2
	v_pk_mul_f16 v6, v5, v6
	v_pk_fma_f16 v118, v1, v2, v0 neg_lo:[1,0,0] neg_hi:[1,0,0]
	v_cvt_pk_f16_f32 v1, v8, v9
	v_exp_f16_e32 v7, v6
	v_exp_f16_sdwa v6, v6 dst_sel:DWORD dst_unused:UNUSED_PAD src0_sel:WORD_1
	v_and_b32_e32 v2, 0x7fff7fff, v1
	v_pk_fma_f16 v3, v2, s2, v164 op_sel_hi:[1,0,0]
	v_mfma_f32_32x32x16_f16 v[16:31], v[88:91], v[104:107], v[16:31]
	v_pk_fma_f16 v3, v3, v2, s3 op_sel_hi:[1,1,0]
	v_pack_b32_f16 v0, v7, v6
	v_pk_mul_f16 v3, v2, v3
	v_pk_add_f16 v4, v5, v4
	v_exp_f16_e32 v6, v3
	v_exp_f16_sdwa v3, v3 dst_sel:DWORD dst_unused:UNUSED_PAD src0_sel:WORD_1
	v_pk_fma_f16 v119, v5, v0, v4 neg_lo:[1,0,0] neg_hi:[1,0,0]
	v_cvt_pk_f16_f32 v4, v10, v11
	v_pk_add_f16 v1, v2, v1
	v_pack_b32_f16 v0, v6, v3
	v_and_b32_e32 v5, 0x7fff7fff, v4
	v_pk_fma_f16 v124, v2, v0, v1 neg_lo:[1,0,0] neg_hi:[1,0,0]
	v_pk_fma_f16 v0, v5, s2, v164 op_sel_hi:[1,0,0]
	v_mfma_f32_32x32x16_f16 v[16:31], v[84:87], v[100:103], v[16:31]
	v_pk_fma_f16 v0, v0, v5, s3 op_sel_hi:[1,1,0]
	v_addc_co_u32_e32 v137, vcc, 0, v157, vcc
	v_pk_mul_f16 v0, v5, v0
	ds_read_b128 v[84:87], v253 offset:43648
	v_exp_f16_e32 v6, v0
	v_exp_f16_sdwa v7, v0 dst_sel:DWORD dst_unused:UNUSED_PAD src0_sel:WORD_1
	ds_read_b128 v[0:3], v254 offset:3072
	s_waitcnt vmcnt(0) lgkmcnt(6)
	v_mfma_f32_32x32x16_f16 v[16:31], v[126:129], v[112:115], v[16:31]
	s_mov_b32 s6, 0xb000
	v_cvt_pk_f16_f32 v8, v12, v13
	v_and_b32_e32 v9, 0x7fff7fff, v8
	v_pk_fma_f16 v10, v9, s2, v164 op_sel_hi:[1,0,0]
	v_pack_b32_f16 v6, v6, v7
	v_pk_fma_f16 v10, v10, v9, s3 op_sel_hi:[1,1,0]
	v_pk_add_f16 v4, v5, v4
	v_mfma_f32_32x32x16_f16 v[16:31], v[144:147], v[108:111], v[16:31]
	v_pk_mul_f16 v10, v9, v10
	v_pk_fma_f16 v125, v5, v6, v4 neg_lo:[1,0,0] neg_hi:[1,0,0]
	v_exp_f16_e32 v11, v10
	v_exp_f16_sdwa v10, v10 dst_sel:DWORD dst_unused:UNUSED_PAD src0_sel:WORD_1
	v_pk_add_f16 v5, v9, v8
	v_pack_b32_f16 v4, v11, v10
	v_mfma_f32_32x32x16_f16 v[16:31], v[120:123], v[48:51], v[16:31]
	v_pk_fma_f16 v126, v9, v4, v5 neg_lo:[1,0,0] neg_hi:[1,0,0]
	v_cvt_pk_f16_f32 v4, v14, v15
	v_and_b32_e32 v5, 0x7fff7fff, v4
	v_pk_fma_f16 v6, v5, s2, v164 op_sel_hi:[1,0,0]
	v_pk_add_f16 v4, v5, v4
	v_pk_fma_f16 v6, v6, v5, s3 op_sel_hi:[1,1,0]
	v_mfma_f32_32x32x16_f16 v[16:31], v[148:151], v[52:55], v[16:31]
	v_add_co_u32_e32 v150, vcc, s7, v156
	v_pk_mul_f16 v6, v5, v6
	s_nop 0
	v_addc_co_u32_e32 v151, vcc, 0, v157, vcc
	ds_read_b128 v[88:91], v253 offset:45696
	v_add_co_u32_e32 v152, vcc, s6, v156
	v_mfma_f32_32x32x16_f16 v[16:31], v[36:39], v[56:59], v[16:31]
	s_nop 0
	v_addc_co_u32_e32 v153, vcc, 0, v157, vcc
	ds_read_b128 v[92:95], v253 offset:47744
	ds_read_b128 v[146:149], v253 offset:48768
	ds_read_b128 v[120:123], v253 offset:51840
	ds_read_b128 v[166:169], v253 offset:50816
	v_exp_f16_e32 v7, v6
	s_waitcnt vmcnt(0) lgkmcnt(10)
	v_mfma_f32_32x32x16_f16 v[16:31], v[64:67], v[60:63], v[16:31]
	ds_read_b128 v[64:67], v253 offset:49792
	v_exp_f16_sdwa v6, v6 dst_sel:DWORD dst_unused:UNUSED_PAD src0_sel:WORD_1
	s_mov_b32 s6, 0xe000
	v_add_co_u32_e32 v138, vcc, s6, v156
	v_pack_b32_f16 v6, v7, v6
	v_pk_fma_f16 v127, v5, v6, v4 neg_lo:[1,0,0] neg_hi:[1,0,0]
	s_nop 5
	v_cvt_pk_f16_f32 v8, v16, v17
	v_and_b32_e32 v9, 0x7fff7fff, v8
	v_pk_fma_f16 v10, v9, s2, v164 op_sel_hi:[1,0,0]
	v_pk_add_f16 v5, v9, v8
	v_pk_fma_f16 v10, v10, v9, s3 op_sel_hi:[1,1,0]
	v_addc_co_u32_e32 v139, vcc, 0, v157, vcc
	v_pk_mul_f16 v10, v9, v10
	v_cvt_pk_f16_f32 v8, v20, v21
	v_exp_f16_e32 v11, v10
	v_exp_f16_sdwa v10, v10 dst_sel:DWORD dst_unused:UNUSED_PAD src0_sel:WORD_1
	v_and_b32_e32 v20, 0x7fff7fff, v8
	v_pk_add_f16 v82, v20, v8
	ds_read_b128 v[36:39], v254 offset:2048
	v_pack_b32_f16 v4, v11, v10
	v_pk_fma_f16 v128, v9, v4, v5 neg_lo:[1,0,0] neg_hi:[1,0,0]
	v_cvt_pk_f16_f32 v4, v18, v19
	ds_read_b128 v[16:19], v254 offset:1024
	v_and_b32_e32 v5, 0x7fff7fff, v4
	v_pk_fma_f16 v6, v5, s2, v164 op_sel_hi:[1,0,0]
	v_pk_fma_f16 v9, v20, s2, v164 op_sel_hi:[1,0,0]
	v_pk_fma_f16 v6, v6, v5, s3 op_sel_hi:[1,1,0]
	v_pk_fma_f16 v9, v9, v20, s3 op_sel_hi:[1,1,0]
	v_pk_mul_f16 v6, v5, v6
	v_pk_mul_f16 v9, v20, v9
	v_exp_f16_e32 v7, v6
	v_exp_f16_sdwa v6, v6 dst_sel:DWORD dst_unused:UNUSED_PAD src0_sel:WORD_1
	v_exp_f16_e32 v10, v9
	v_exp_f16_sdwa v9, v9 dst_sel:DWORD dst_unused:UNUSED_PAD src0_sel:WORD_1
	v_pk_add_f16 v4, v5, v4
	v_pack_b32_f16 v6, v7, v6
	v_pk_fma_f16 v129, v5, v6, v4 neg_lo:[1,0,0] neg_hi:[1,0,0]
	v_pack_b32_f16 v21, v10, v9
	s_waitcnt vmcnt(0) lgkmcnt(8)
	v_mfma_f32_32x32x16_f16 v[0:15], v[0:3], v[96:99], 0
	v_pk_fma_f16 v130, v20, v21, v82 neg_lo:[1,0,0] neg_hi:[1,0,0]
	v_cvt_pk_f16_f32 v82, v22, v23
	v_and_b32_e32 v131, 0x7fff7fff, v82
	v_pk_fma_f16 v20, v131, s2, v164 op_sel_hi:[1,0,0]
	v_cvt_pk_f16_f32 v24, v24, v25
	v_pk_fma_f16 v20, v20, v131, s3 op_sel_hi:[1,1,0]
	v_and_b32_e32 v25, 0x7fff7fff, v24
	v_pk_mul_f16 v20, v131, v20
	v_mfma_f32_32x32x16_f16 v[0:15], v[132:135], v[104:107], v[0:15]
	v_exp_f16_e32 v144, v20
	v_exp_f16_sdwa v132, v20 dst_sel:DWORD dst_unused:UNUSED_PAD src0_sel:WORD_1
	v_pk_fma_f16 v20, v25, s2, v164 op_sel_hi:[1,0,0]
	ds_read_b128 v[152:155], v253 offset:46720
	v_pk_fma_f16 v20, v20, v25, s3 op_sel_hi:[1,1,0]
	v_pack_b32_f16 v132, v144, v132
	v_pk_mul_f16 v133, v25, v20
	ds_read_b128 v[20:23], v254 offset:4096
	v_mfma_f32_32x32x16_f16 v[0:15], v[140:143], v[100:103], v[0:15]
	ds_read_b128 v[142:145], v253 offset:42624
	v_cvt_pk_f16_f32 v26, v26, v27
	v_and_b32_e32 v27, 0x7fff7fff, v26
	v_exp_f16_e32 v134, v133
	v_exp_f16_sdwa v133, v133 dst_sel:DWORD dst_unused:UNUSED_PAD src0_sel:WORD_1
	v_pk_add_f16 v82, v131, v82
	v_pk_add_f16 v24, v25, v24
	v_mfma_f32_32x32x16_f16 v[0:15], v[84:87], v[112:115], v[0:15]
	v_pk_fma_f16 v84, v27, s2, v164 op_sel_hi:[1,0,0]
	v_pk_fma_f16 v131, v131, v132, v82 neg_lo:[1,0,0] neg_hi:[1,0,0]
	v_pk_fma_f16 v84, v84, v27, s3 op_sel_hi:[1,1,0]
	v_pack_b32_f16 v82, v134, v133
	v_pk_mul_f16 v84, v27, v84
	v_pk_fma_f16 v132, v25, v82, v24 neg_lo:[1,0,0] neg_hi:[1,0,0]
	v_exp_f16_e32 v85, v84
	s_waitcnt vmcnt(0) lgkmcnt(10)
	v_mfma_f32_32x32x16_f16 v[0:15], v[88:91], v[108:111], v[0:15]
	v_exp_f16_sdwa v84, v84 dst_sel:DWORD dst_unused:UNUSED_PAD src0_sel:WORD_1
	v_pk_add_f16 v25, v27, v26
	ds_read_b128 v[170:173], v254
	s_mov_b32 s6, 0x13000
	v_pack_b32_f16 v24, v85, v84
	v_pk_fma_f16 v133, v27, v24, v25 neg_lo:[1,0,0] neg_hi:[1,0,0]
	v_cvt_pk_f16_f32 v24, v28, v29
	s_waitcnt vmcnt(0) lgkmcnt(10)
	v_mfma_f32_32x32x16_f16 v[0:15], v[92:95], v[72:75], v[0:15]
	v_and_b32_e32 v25, 0x7fff7fff, v24
	v_cvt_pk_f16_f32 v28, v30, v31
	v_pk_fma_f16 v26, v25, s2, v164 op_sel_hi:[1,0,0]
	v_and_b32_e32 v29, 0x7fff7fff, v28
	v_pk_fma_f16 v26, v26, v25, s3 op_sel_hi:[1,1,0]
	v_pk_fma_f16 v30, v29, s2, v164 op_sel_hi:[1,0,0]
	v_pk_mul_f16 v26, v25, v26
	s_waitcnt vmcnt(0) lgkmcnt(6)
	v_mfma_f32_32x32x16_f16 v[0:15], v[64:67], v[68:71], v[0:15]
	v_pk_fma_f16 v30, v30, v29, s3 op_sel_hi:[1,1,0]
	v_exp_f16_e32 v27, v26
	v_exp_f16_sdwa v26, v26 dst_sel:DWORD dst_unused:UNUSED_PAD src0_sel:WORD_1
	v_pk_mul_f16 v30, v29, v30
	v_pk_add_f16 v24, v25, v24
	v_exp_f16_e32 v31, v30
	v_exp_f16_sdwa v30, v30 dst_sel:DWORD dst_unused:UNUSED_PAD src0_sel:WORD_1
	v_mfma_f32_32x32x16_f16 v[0:15], v[120:123], v[40:43], v[0:15]
	v_pack_b32_f16 v26, v27, v26
	v_pk_fma_f16 v134, v25, v26, v24 neg_lo:[1,0,0] neg_hi:[1,0,0]
	v_pack_b32_f16 v24, v31, v30
	v_pk_add_f16 v25, v29, v28
	v_add_co_u32_e32 v150, vcc, s6, v156
	v_pk_fma_f16 v135, v29, v24, v25 neg_lo:[1,0,0] neg_hi:[1,0,0]
	s_waitcnt vmcnt(0) lgkmcnt(4)
	v_mfma_f32_32x32x16_f16 v[0:15], v[16:19], v[32:35], v[0:15]
	v_addc_co_u32_e32 v151, vcc, 0, v157, vcc
	ds_read_b128 v[64:67], v254 offset:5120
	ds_read_b128 v[84:87], v254 offset:7168
	s_mov_b32 s6, 0x10000
	v_add_co_u32_e32 v140, vcc, s6, v156
	s_nop 6
	v_cvt_pk_f16_f32 v16, v0, v1
	v_and_b32_e32 v17, 0x7fff7fff, v16
	v_pk_fma_f16 v0, v17, s2, v164 op_sel_hi:[1,0,0]
	v_cvt_pk_f16_f32 v24, v2, v3
	v_pk_fma_f16 v0, v0, v17, s3 op_sel_hi:[1,1,0]
	v_and_b32_e32 v25, 0x7fff7fff, v24
	v_pk_mul_f16 v0, v17, v0
	v_pk_add_f16 v16, v17, v16
	v_exp_f16_e32 v18, v0
	v_exp_f16_sdwa v19, v0 dst_sel:DWORD dst_unused:UNUSED_PAD src0_sel:WORD_1
	v_pk_fma_f16 v0, v25, s2, v164 op_sel_hi:[1,0,0]
	v_addc_co_u32_e32 v141, vcc, 0, v157, vcc
	v_pk_fma_f16 v0, v0, v25, s3 op_sel_hi:[1,1,0]
	v_pack_b32_f16 v18, v18, v19
	v_pk_mul_f16 v26, v25, v0
	ds_read_b128 v[0:3], v254 offset:21824
	v_exp_f16_e32 v27, v26
	v_exp_f16_sdwa v26, v26 dst_sel:DWORD dst_unused:UNUSED_PAD src0_sel:WORD_1
	v_pk_fma_f16 v120, v17, v18, v16 neg_lo:[1,0,0] neg_hi:[1,0,0]
	v_pk_add_f16 v17, v25, v24
	ds_read_b128 v[88:91], v254 offset:9216
	v_pack_b32_f16 v16, v27, v26
	v_pk_fma_f16 v121, v25, v16, v17 neg_lo:[1,0,0] neg_hi:[1,0,0]
	s_waitcnt vmcnt(0) lgkmcnt(6)
	v_mfma_f32_32x32x16_f16 v[16:31], v[20:23], v[96:99], 0
	v_cvt_pk_f16_f32 v82, v4, v5
	s_mov_b32 s6, 0xf000
	v_and_b32_e32 v122, 0x7fff7fff, v82
	v_add_co_u32_e32 v162, vcc, s6, v156
	v_pk_fma_f16 v4, v122, s2, v164 op_sel_hi:[1,0,0]
	s_nop 0
	v_addc_co_u32_e32 v163, vcc, 0, v157, vcc
	v_mfma_f32_32x32x16_f16 v[16:31], v[44:47], v[104:107], v[16:31]
	v_pk_fma_f16 v4, v4, v122, s3 op_sel_hi:[1,1,0]
	ds_read_b128 v[92:95], v254 offset:11264
	v_pk_mul_f16 v4, v122, v4
	v_cvt_pk_f16_f32 v45, v6, v7
	v_exp_f16_e32 v5, v4
	v_exp_f16_sdwa v4, v4 dst_sel:DWORD dst_unused:UNUSED_PAD src0_sel:WORD_1
	v_and_b32_e32 v46, 0x7fff7fff, v45
	s_waitcnt vmcnt(0) lgkmcnt(6)
	v_mfma_f32_32x32x16_f16 v[16:31], v[142:145], v[100:103], v[16:31]
	s_mov_b32 s6, 0x11000
	v_pack_b32_f16 v44, v5, v4
	v_pk_fma_f16 v4, v46, s2, v164 op_sel_hi:[1,0,0]
	v_cvt_pk_f16_f32 v10, v10, v11
	v_pk_fma_f16 v4, v4, v46, s3 op_sel_hi:[1,1,0]
	v_and_b32_e32 v11, 0x7fff7fff, v10
	v_pk_mul_f16 v47, v46, v4
	v_mfma_f32_32x32x16_f16 v[16:31], v[76:79], v[112:115], v[16:31]
	ds_read_b128 v[4:7], v254 offset:13312
	v_exp_f16_e32 v76, v47
	v_exp_f16_sdwa v47, v47 dst_sel:DWORD dst_unused:UNUSED_PAD src0_sel:WORD_1
	v_pk_add_f16 v77, v122, v82
	v_pk_add_f16 v45, v46, v45
	v_pk_fma_f16 v122, v122, v44, v77 neg_lo:[1,0,0] neg_hi:[1,0,0]
	v_pack_b32_f16 v44, v76, v47
	v_mfma_f32_32x32x16_f16 v[16:31], v[152:155], v[108:111], v[16:31]
	ds_read_b128 v[76:79], v254 offset:15360
	v_cvt_pk_f16_f32 v47, v8, v9
	v_add_co_u32_e32 v8, vcc, s6, v156
	v_and_b32_e32 v82, 0x7fff7fff, v47
	s_nop 0
	v_addc_co_u32_e32 v9, vcc, 0, v157, vcc
	v_mfma_f32_32x32x16_f16 v[16:31], v[146:149], v[72:75], v[16:31]
	ds_read_b128 v[72:75], v254 offset:17728
	v_pk_fma_f16 v123, v82, s2, v164 op_sel_hi:[1,0,0]
	s_mov_b32 s6, 0x12000
	v_pk_fma_f16 v123, v123, v82, s3 op_sel_hi:[1,1,0]
	v_add_co_u32_e32 v160, vcc, s6, v156
	ds_read_b128 v[146:149], v254 offset:6144
	v_mfma_f32_32x32x16_f16 v[16:31], v[166:169], v[68:71], v[16:31]
	v_pk_mul_f16 v68, v82, v123
	v_addc_co_u32_e32 v161, vcc, 0, v157, vcc
	v_exp_f16_e32 v136, v68
	v_exp_f16_sdwa v137, v68 dst_sel:DWORD dst_unused:UNUSED_PAD src0_sel:WORD_1
	ds_read_b128 v[68:71], v254 offset:19776
	ds_read_b128 v[142:145], v254 offset:22848
	s_waitcnt vmcnt(0) lgkmcnt(11)
	v_mfma_f32_32x32x16_f16 v[16:31], v[170:173], v[40:43], v[16:31]
	v_pk_fma_f16 v123, v46, v44, v45 neg_lo:[1,0,0] neg_hi:[1,0,0]
	v_pack_b32_f16 v136, v136, v137
	v_pk_add_f16 v137, v82, v47
	ds_read_b128 v[170:173], v254 offset:16384
	v_pk_fma_f16 v136, v82, v136, v137 neg_lo:[1,0,0] neg_hi:[1,0,0]
	s_mov_b32 s6, 0x16000
	ds_read_b128 v[152:155], v254 offset:25920
	v_mfma_f32_32x32x16_f16 v[16:31], v[36:39], v[32:35], v[16:31]
	v_pk_fma_f16 v32, v11, s2, v164 op_sel_hi:[1,0,0]
	s_nop 0
	v_pk_fma_f16 v32, v32, v11, s3 op_sel_hi:[1,1,0]
	s_nop 0
	v_pk_mul_f16 v32, v11, v32
	s_nop 6
	v_cvt_pk_f16_f32 v24, v24, v25
	v_exp_f16_e32 v165, v32
	v_exp_f16_sdwa v166, v32 dst_sel:DWORD dst_unused:UNUSED_PAD src0_sel:WORD_1
	s_waitcnt vmcnt(0) lgkmcnt(10)
	v_mfma_f32_32x32x16_f16 v[32:47], v[0:3], v[96:99], 0
	v_pk_add_f16 v1, v11, v10
	v_cvt_pk_f16_f32 v10, v14, v15
	v_pack_b32_f16 v0, v165, v166
	ds_read_b128 v[166:169], v254 offset:8192
	v_pk_fma_f16 v137, v11, v0, v1 neg_lo:[1,0,0] neg_hi:[1,0,0]
	v_cvt_pk_f16_f32 v0, v12, v13
	v_and_b32_e32 v1, 0x7fff7fff, v0
	v_mfma_f32_32x32x16_f16 v[32:47], v[64:67], v[104:107], v[32:47]
	ds_read_b128 v[64:67], v254 offset:10240
	v_pk_fma_f16 v2, v1, s2, v164 op_sel_hi:[1,0,0]
	v_and_b32_e32 v11, 0x7fff7fff, v10
	v_pk_fma_f16 v2, v2, v1, s3 op_sel_hi:[1,1,0]
	v_pk_fma_f16 v12, v11, s2, v164 op_sel_hi:[1,0,0]
	v_pk_mul_f16 v2, v1, v2
	v_pk_fma_f16 v12, v12, v11, s3 op_sel_hi:[1,1,0]
	v_mfma_f32_32x32x16_f16 v[32:47], v[84:87], v[100:103], v[32:47]
	v_exp_f16_e32 v3, v2
	v_exp_f16_sdwa v2, v2 dst_sel:DWORD dst_unused:UNUSED_PAD src0_sel:WORD_1
	v_pk_mul_f16 v12, v11, v12
	v_pk_add_f16 v0, v1, v0
	v_exp_f16_e32 v13, v12
	v_exp_f16_sdwa v12, v12 dst_sel:DWORD dst_unused:UNUSED_PAD src0_sel:WORD_1
	v_pack_b32_f16 v2, v3, v2
	s_waitcnt vmcnt(0) lgkmcnt(11)
	v_mfma_f32_32x32x16_f16 v[32:47], v[88:91], v[112:115], v[32:47]
	ds_read_b128 v[88:91], v254 offset:12288
	v_pk_fma_f16 v138, v1, v2, v0 neg_lo:[1,0,0] neg_hi:[1,0,0]
	v_pack_b32_f16 v0, v13, v12
	v_pk_add_f16 v1, v11, v10
	v_add_co_u32_e32 v162, vcc, s6, v156
	v_pk_fma_f16 v139, v11, v0, v1 neg_lo:[1,0,0] neg_hi:[1,0,0]
	s_waitcnt vmcnt(0) lgkmcnt(11)
	v_mfma_f32_32x32x16_f16 v[32:47], v[92:95], v[108:111], v[32:47]
	ds_read_b128 v[92:95], v254 offset:14336
	v_cvt_pk_f16_f32 v0, v16, v17
	v_and_b32_e32 v1, 0x7fff7fff, v0
	v_pk_fma_f16 v2, v1, s2, v164 op_sel_hi:[1,0,0]
	v_pk_add_f16 v0, v1, v0
	v_pk_fma_f16 v2, v2, v1, s3 op_sel_hi:[1,1,0]
	v_addc_co_u32_e32 v163, vcc, 0, v157, vcc
	s_waitcnt vmcnt(0) lgkmcnt(11)
	v_mfma_f32_32x32x16_f16 v[32:47], v[4:7], v[48:51], v[32:47]
	v_cvt_pk_f16_f32 v4, v18, v19
	v_and_b32_e32 v5, 0x7fff7fff, v4
	ds_read_b128 v[16:19], v254 offset:18752
	v_pk_fma_f16 v6, v5, s2, v164 op_sel_hi:[1,0,0]
	v_pk_mul_f16 v2, v1, v2
	v_pk_fma_f16 v6, v6, v5, s3 op_sel_hi:[1,1,0]
	v_exp_f16_e32 v3, v2
	s_waitcnt vmcnt(0) lgkmcnt(11)
	v_mfma_f32_32x32x16_f16 v[32:47], v[76:79], v[52:55], v[32:47]
	v_exp_f16_sdwa v2, v2 dst_sel:DWORD dst_unused:UNUSED_PAD src0_sel:WORD_1
	v_pk_mul_f16 v6, v5, v6
	ds_read_b128 v[84:87], v254 offset:28992
	v_exp_f16_e32 v7, v6
	v_exp_f16_sdwa v6, v6 dst_sel:DWORD dst_unused:UNUSED_PAD src0_sel:WORD_1
	v_pack_b32_f16 v2, v3, v2
	v_pk_fma_f16 v140, v1, v2, v0 neg_lo:[1,0,0] neg_hi:[1,0,0]
	s_waitcnt vmcnt(0) lgkmcnt(11)
	v_mfma_f32_32x32x16_f16 v[32:47], v[72:75], v[56:59], v[32:47]
	v_pack_b32_f16 v0, v7, v6
	ds_read_b128 v[72:75], v254 offset:20800
	v_pk_add_f16 v1, v5, v4
	s_mov_b32 s6, 0x14000
	v_pk_fma_f16 v141, v5, v0, v1 neg_lo:[1,0,0] neg_hi:[1,0,0]
	v_lshlrev_b32_e32 v0, 2, v159
	v_ashrrev_i32_e32 v1, 31, v0
	v_lshl_add_u64 v[0:1], v[0:1], 2, v[80:81]
	global_load_dwordx4 v[76:79], v[0:1], off
	s_waitcnt vmcnt(1) lgkmcnt(10)
	v_mfma_f32_32x32x16_f16 v[32:47], v[68:71], v[60:63], v[32:47]
	ds_read_b128 v[68:71], v254 offset:40576
	ds_read_b128 v[174:177], v254 offset:23872
	s_waitcnt vmcnt(0) lgkmcnt(2)
	v_cvt_pk_f16_f32 v79, v20, v21
	v_and_b32_e32 v80, 0x7fff7fff, v79
	v_pk_fma_f16 v20, v80, s2, v164 op_sel_hi:[1,0,0]
	v_pk_add_f16 v79, v80, v79
	v_pk_fma_f16 v20, v20, v80, s3 op_sel_hi:[1,1,0]
	v_and_b32_e32 v25, 0x7fff7fff, v24
	v_mfma_f32_32x32x16_f16 v[0:15], v[142:145], v[96:99], 0
	v_cvt_pk_f16_f32 v143, v22, v23
	v_pk_mul_f16 v20, v80, v20
	v_and_b32_e32 v144, 0x7fff7fff, v143
	v_exp_f16_e32 v81, v20
	v_exp_f16_sdwa v82, v20 dst_sel:DWORD dst_unused:UNUSED_PAD src0_sel:WORD_1
	v_pk_fma_f16 v20, v144, s2, v164 op_sel_hi:[1,0,0]
	v_cvt_pk_f16_f32 v26, v26, v27
	v_pk_fma_f16 v20, v20, v144, s3 op_sel_hi:[1,1,0]
	v_mfma_f32_32x32x16_f16 v[0:15], v[146:149], v[104:107], v[0:15]
	v_pk_mul_f16 v142, v144, v20
	ds_read_b128 v[20:23], v254 offset:27968
	v_add_co_u32_e32 v148, vcc, s6, v156
	s_mov_b32 s6, 0x15000
	s_nop 0
	v_addc_co_u32_e32 v149, vcc, 0, v157, vcc
	v_mfma_f32_32x32x16_f16 v[0:15], v[166:169], v[100:103], v[0:15]
	ds_read_b128 v[166:169], v254 offset:32064
	ds_read_b128 v[178:181], v254 offset:24896
	v_add_co_u32_e32 v194, vcc, s6, v156
	v_exp_f16_e32 v145, v142
	s_nop 0
	v_addc_co_u32_e32 v195, vcc, 0, v157, vcc
	v_exp_f16_sdwa v146, v142 dst_sel:DWORD dst_unused:UNUSED_PAD src0_sel:WORD_1
	v_mfma_f32_32x32x16_f16 v[0:15], v[64:67], v[112:115], v[0:15]
	ds_read_b128 v[64:67], v254 offset:36480
	v_pack_b32_f16 v81, v81, v82
	v_pk_fma_f16 v142, v80, v81, v79 neg_lo:[1,0,0] neg_hi:[1,0,0]
	v_pack_b32_f16 v79, v145, v146
	v_pk_add_f16 v80, v144, v143
	s_mov_b32 s6, 0x18000
	v_pk_fma_f16 v143, v144, v79, v80 neg_lo:[1,0,0] neg_hi:[1,0,0]
	v_mfma_f32_32x32x16_f16 v[0:15], v[88:91], v[108:111], v[0:15]
	ds_read_b128 v[88:91], v254 offset:41600
	v_pk_fma_f16 v79, v25, s2, v164 op_sel_hi:[1,0,0]
	v_add_co_u32_e32 v160, vcc, s6, v156
	v_pk_fma_f16 v79, v79, v25, s3 op_sel_hi:[1,1,0]
	v_pk_add_f16 v24, v25, v24
	v_pk_mul_f16 v79, v25, v79
	v_mfma_f32_32x32x16_f16 v[0:15], v[92:95], v[48:51], v[0:15]
	ds_read_b128 v[92:95], v254 offset:33088
	ds_read_b128 v[186:189], v254 offset:31040
	v_exp_f16_e32 v48, v79
	v_exp_f16_sdwa v49, v79 dst_sel:DWORD dst_unused:UNUSED_PAD src0_sel:WORD_1
	v_addc_co_u32_e32 v161, vcc, 0, v157, vcc
	v_and_b32_e32 v27, 0x7fff7fff, v26
	v_mfma_f32_32x32x16_f16 v[0:15], v[170:173], v[52:55], v[0:15]
	v_pack_b32_f16 v48, v48, v49
	v_pk_fma_f16 v144, v25, v48, v24 neg_lo:[1,0,0] neg_hi:[1,0,0]
	v_cvt_pk_f16_f32 v25, v28, v29
	v_pk_fma_f16 v50, v27, s2, v164 op_sel_hi:[1,0,0]
	v_mov_b32_e32 v82, v83
	v_pk_fma_f16 v50, v50, v27, s3 op_sel_hi:[1,1,0]
	ds_read_b128 v[170:173], v254 offset:30016
	v_mfma_f32_32x32x16_f16 v[0:15], v[16:19], v[56:59], v[0:15]
	v_pk_mul_f16 v50, v27, v50
	ds_read_b128 v[182:185], v254 offset:34112
	v_exp_f16_e32 v51, v50
	v_exp_f16_sdwa v50, v50 dst_sel:DWORD dst_unused:UNUSED_PAD src0_sel:WORD_1
	v_and_b32_e32 v16, 0x7fff7fff, v25
	v_pk_fma_f16 v17, v16, s2, v164 op_sel_hi:[1,0,0]
	s_mov_b32 s6, 0x17000
	v_mfma_f32_32x32x16_f16 v[0:15], v[72:75], v[60:63], v[0:15]
	ds_read_b128 v[72:75], v254 offset:37504
	v_pack_b32_f16 v24, v51, v50
	v_cvt_pk_f16_f32 v19, v76, v77
	v_cvt_pk_f16_f32 v28, v78, 1.0
	ds_read_b128 v[76:79], v254 offset:42624
	v_cndmask_b32_e64 v80, 0, v19, s[4:5]
	v_cndmask_b32_e64 v81, 0, v28, s[4:5]
	v_pk_fma_f16 v17, v17, v16, s3 op_sel_hi:[1,1,0]
	v_add_co_u32_e32 v202, vcc, s6, v156
	s_waitcnt vmcnt(0) lgkmcnt(12)
	v_mfma_f32_32x32x16_f16 v[48:63], v[68:71], v[80:83], 0
	v_pk_mul_f16 v17, v16, v17
	v_addc_co_u32_e32 v203, vcc, 0, v157, vcc
	v_exp_f16_e32 v18, v17
	v_exp_f16_sdwa v17, v17 dst_sel:DWORD dst_unused:UNUSED_PAD src0_sel:WORD_1
	ds_read_b128 v[190:193], v254 offset:43648
	v_pk_add_f16 v19, v27, v26
	s_waitcnt vmcnt(0) lgkmcnt(12)
	v_mfma_f32_32x32x16_f16 v[48:63], v[174:177], v[116:119], v[48:63]
	v_pk_fma_f16 v145, v27, v24, v19 neg_lo:[1,0,0] neg_hi:[1,0,0]
	v_pack_b32_f16 v17, v18, v17
	v_pk_add_f16 v18, v16, v25
	v_cvt_pk_f16_f32 v19, v30, v31
	v_and_b32_e32 v24, 0x7fff7fff, v19
	v_pk_fma_f16 v146, v16, v17, v18 neg_lo:[1,0,0] neg_hi:[1,0,0]
	v_cvt_pk_f16_f32 v17, v32, v33
	s_waitcnt vmcnt(0) lgkmcnt(11)
	v_mfma_f32_32x32x16_f16 v[48:63], v[20:23], v[124:127], v[48:63]
	v_pk_fma_f16 v25, v24, s2, v164 op_sel_hi:[1,0,0]
	v_and_b32_e32 v32, 0x7fff7fff, v17
	v_pk_fma_f16 v25, v25, v24, s3 op_sel_hi:[1,1,0]
	v_pk_fma_f16 v18, v32, s2, v164 op_sel_hi:[1,0,0]
	v_pk_mul_f16 v25, v24, v25
	v_pk_fma_f16 v18, v18, v32, s3 op_sel_hi:[1,1,0]
	v_exp_f16_e32 v26, v25
	s_waitcnt vmcnt(0) lgkmcnt(10)
	v_mfma_f32_32x32x16_f16 v[48:63], v[166:169], v[128:131], v[48:63]
	ds_read_b128 v[166:169], v254 offset:38528
	v_exp_f16_sdwa v25, v25 dst_sel:DWORD dst_unused:UNUSED_PAD src0_sel:WORD_1
	ds_read_b128 v[174:177], v254 offset:26944
	v_pk_mul_f16 v18, v32, v18
	v_pk_add_f16 v19, v24, v19
	v_exp_f16_e32 v20, v18
	v_exp_f16_sdwa v18, v18 dst_sel:DWORD dst_unused:UNUSED_PAD src0_sel:WORD_1
	v_pack_b32_f16 v16, v26, v25
	v_pk_fma_f16 v147, v24, v16, v19 neg_lo:[1,0,0] neg_hi:[1,0,0]
	s_waitcnt vmcnt(0) lgkmcnt(10)
	v_mfma_f32_32x32x16_f16 v[48:63], v[64:67], v[132:135], v[48:63]
	v_pack_b32_f16 v33, v20, v18
	v_pk_add_f16 v64, v32, v17
	v_cvt_pk_f16_f32 v36, v36, v37
	v_pk_fma_f16 v148, v32, v33, v64 neg_lo:[1,0,0] neg_hi:[1,0,0]
	v_cvt_pk_f16_f32 v32, v34, v35
	v_and_b32_e32 v33, 0x7fff7fff, v32
	v_pk_fma_f16 v34, v33, s2, v164 op_sel_hi:[1,0,0]
	s_waitcnt vmcnt(0) lgkmcnt(9)
	v_mfma_f32_32x32x16_f16 v[16:31], v[88:91], v[80:83], 0
	v_pk_fma_f16 v34, v34, v33, s3 op_sel_hi:[1,1,0]
	v_and_b32_e32 v37, 0x7fff7fff, v36
	v_pk_mul_f16 v34, v33, v34
	v_pk_add_f16 v32, v33, v32
	v_exp_f16_e32 v35, v34
	v_exp_f16_sdwa v34, v34 dst_sel:DWORD dst_unused:UNUSED_PAD src0_sel:WORD_1
	v_pk_fma_f16 v64, v37, s2, v164 op_sel_hi:[1,0,0]
	v_mfma_f32_32x32x16_f16 v[16:31], v[178:181], v[116:119], v[16:31]
	v_pk_fma_f16 v64, v64, v37, s3 op_sel_hi:[1,1,0]
	v_pack_b32_f16 v34, v35, v34
	v_pk_fma_f16 v149, v33, v34, v32 neg_lo:[1,0,0] neg_hi:[1,0,0]
	ds_read_b128 v[32:35], v254 offset:35456
	v_pk_mul_f16 v64, v37, v64
	v_pk_add_f16 v36, v37, v36
	v_exp_f16_e32 v65, v64
	v_exp_f16_sdwa v64, v64 dst_sel:DWORD dst_unused:UNUSED_PAD src0_sel:WORD_1
	v_mfma_f32_32x32x16_f16 v[16:31], v[84:87], v[124:127], v[16:31]
	v_cvt_pk_f16_f32 v84, v38, v39
	v_and_b32_e32 v85, 0x7fff7fff, v84
	v_pack_b32_f16 v64, v65, v64
	v_pk_fma_f16 v150, v37, v64, v36 neg_lo:[1,0,0] neg_hi:[1,0,0]
	v_pk_fma_f16 v36, v85, s2, v164 op_sel_hi:[1,0,0]
	s_mov_b32 s6, 0x1b000
	v_pk_fma_f16 v64, v36, v85, s3 op_sel_hi:[1,1,0]
	ds_read_b128 v[36:39], v254 offset:39552
	s_waitcnt vmcnt(0) lgkmcnt(10)
	v_mfma_f32_32x32x16_f16 v[16:31], v[92:95], v[128:131], v[16:31]
	v_add_co_u32_e32 v204, vcc, s6, v156
	v_pk_mul_f16 v86, v85, v64
	s_nop 0
	v_addc_co_u32_e32 v205, vcc, 0, v157, vcc
	ds_read_b128 v[178:181], v255 offset:8192
	ds_read_b128 v[194:197], v254 offset:46720
	ds_read_b128 v[198:201], v254 offset:44672
	s_waitcnt vmcnt(0) lgkmcnt(9)
	v_mfma_f32_32x32x16_f16 v[16:31], v[72:75], v[132:135], v[16:31]
	v_cvt_pk_f16_f32 v40, v40, v41
	v_and_b32_e32 v41, 0x7fff7fff, v40
	v_pk_fma_f16 v88, v41, s2, v164 op_sel_hi:[1,0,0]
	v_exp_f16_e32 v87, v86
	v_pk_fma_f16 v88, v88, v41, s3 op_sel_hi:[1,1,0]
	v_exp_f16_sdwa v86, v86 dst_sel:DWORD dst_unused:UNUSED_PAD src0_sel:WORD_1
	v_pk_mul_f16 v88, v41, v88
	s_waitcnt vmcnt(0) lgkmcnt(8)
	v_mfma_f32_32x32x16_f16 v[64:79], v[76:79], v[80:83], 0
	v_exp_f16_e32 v89, v88
	v_exp_f16_sdwa v88, v88 dst_sel:DWORD dst_unused:UNUSED_PAD src0_sel:WORD_1
	v_pack_b32_f16 v86, v87, v86
	v_pk_add_f16 v84, v85, v84
	v_pk_add_f16 v40, v41, v40
	v_pk_fma_f16 v151, v85, v86, v84 neg_lo:[1,0,0] neg_hi:[1,0,0]
	v_pack_b32_f16 v84, v89, v88
	v_mfma_f32_32x32x16_f16 v[64:79], v[152:155], v[116:119], v[64:79]
	v_pk_fma_f16 v152, v41, v84, v40 neg_lo:[1,0,0] neg_hi:[1,0,0]
	v_cvt_pk_f16_f32 v153, v42, v43
	ds_read_b128 v[40:43], v254 offset:48768
	s_mov_b32 s6, 0x1a000
	v_add_co_u32_e32 v154, vcc, s6, v156
	s_mov_b32 s6, 0x19000
	v_mfma_f32_32x32x16_f16 v[64:79], v[170:173], v[124:127], v[64:79]
	v_addc_co_u32_e32 v155, vcc, 0, v157, vcc
	ds_read_b128 v[170:173], v254 offset:50816
	v_add_co_u32_e32 v162, vcc, s6, v156
	v_and_b32_e32 v159, 0x7fff7fff, v153
	s_nop 0
	v_addc_co_u32_e32 v163, vcc, 0, v157, vcc
	v_mfma_f32_32x32x16_f16 v[64:79], v[182:185], v[128:131], v[64:79]
	v_pk_fma_f16 v84, v159, s2, v164 op_sel_hi:[1,0,0]
	ds_read_b128 v[182:185], v255 offset:2048
	v_pk_fma_f16 v84, v84, v159, s3 op_sel_hi:[1,1,0]
	s_mov_b32 s6, 0x1c000
	v_pk_mul_f16 v84, v159, v84
	v_cvt_pk_f16_f32 v48, v48, v49
	v_exp_f16_e32 v165, v84
	s_waitcnt vmcnt(0) lgkmcnt(9)
	v_mfma_f32_32x32x16_f16 v[64:79], v[166:169], v[132:135], v[64:79]
	ds_read_b128 v[166:169], v255
	v_exp_f16_sdwa v206, v84 dst_sel:DWORD dst_unused:UNUSED_PAD src0_sel:WORD_1
	v_cvt_pk_f16_f32 v49, v50, v51
	v_cvt_pk_f16_f32 v50, v52, v53
	v_cvt_pk_f16_f32 v51, v54, v55
	v_cvt_pk_f16_f32 v24, v24, v25
	v_cvt_pk_f16_f32 v25, v26, v27
	v_mfma_f32_32x32x16_f16 v[80:95], v[190:193], v[80:83], 0
	v_cvt_pk_f16_f32 v26, v28, v29
	v_cvt_pk_f16_f32 v27, v30, v31
	ds_read_b128 v[28:31], v254 offset:49792
	v_cvt_pk_f16_f32 v20, v20, v21
	v_cvt_pk_f16_f32 v21, v22, v23
	v_pk_max_f16 v23, v21, 0
	v_pk_max_f16 v22, v20, 0
	s_waitcnt vmcnt(0) lgkmcnt(10)
	v_mfma_f32_32x32x16_f16 v[80:95], v[174:177], v[116:119], v[80:95]
	ds_read_b128 v[116:119], v255 offset:4096
	v_pk_max_f16 v176, v50, 0
	v_pk_max_f16 v175, v49, 0
	v_pk_max_f16 v174, v48, 0
	v_cvt_pk_f16_f32 v48, v56, v57
	v_cvt_pk_f16_f32 v49, v58, v59
	v_cvt_pk_f16_f32 v50, v60, v61
	v_mfma_f32_32x32x16_f16 v[80:95], v[186:189], v[124:127], v[80:95]
	v_add_co_u32_e32 v186, vcc, s6, v156
	v_pk_max_f16 v177, v51, 0
	s_nop 0
	v_addc_co_u32_e32 v187, vcc, 0, v157, vcc
	ds_read_b128 v[124:127], v255 offset:6144
	v_pk_max_f16 v27, v27, 0
	s_waitcnt vmcnt(0) lgkmcnt(11)
	v_mfma_f32_32x32x16_f16 v[80:95], v[32:35], v[128:131], v[80:95]
	v_cvt_pk_f16_f32 v32, v62, v63
	v_pk_max_f16 v131, v32, 0
	ds_read_b128 v[32:35], v255 offset:9216
	v_pk_max_f16 v130, v50, 0
	v_pk_max_f16 v129, v49, 0
	v_pk_max_f16 v128, v48, 0
	v_pk_max_f16 v26, v26, 0
	s_waitcnt vmcnt(0) lgkmcnt(11)
	v_mfma_f32_32x32x16_f16 v[80:95], v[36:39], v[132:135], v[80:95]
	v_cvt_pk_f16_f32 v36, v16, v17
	v_cvt_pk_f16_f32 v37, v18, v19
	ds_read_b128 v[16:19], v254 offset:45696
	ds_read_b128 v[132:135], v254 offset:47744
	v_cvt_pk_f16_f32 v38, v68, v69
	v_cvt_pk_f16_f32 v39, v70, v71
	ds_read_b128 v[68:71], v254 offset:51840
	s_waitcnt vmcnt(0) lgkmcnt(13)
	v_mfma_f32_32x32x16_f16 v[48:63], v[178:181], v[96:99], 0
	v_pk_max_f16 v21, v37, 0
	v_pk_max_f16 v20, v36, 0
	v_cvt_pk_f16_f32 v36, v64, v65
	v_cvt_pk_f16_f32 v37, v66, v67
	v_pk_max_f16 v65, v37, 0
	v_pk_max_f16 v64, v36, 0
	v_cvt_pk_f16_f32 v36, v72, v73
	s_waitcnt vmcnt(0) lgkmcnt(11)
	v_mfma_f32_32x32x16_f16 v[48:63], v[198:201], v[174:177], v[48:63]
	v_cvt_pk_f16_f32 v37, v74, v75
	ds_read_b128 v[72:75], v255 offset:1024
	v_pk_max_f16 v25, v25, 0
	v_pk_max_f16 v24, v24, 0
	v_pk_max_f16 v67, v39, 0
	v_pk_max_f16 v66, v38, 0
	ds_read_b128 v[160:163], v255 offset:3072
	v_mfma_f32_32x32x16_f16 v[48:63], v[194:197], v[128:131], v[48:63]
	v_cvt_pk_f16_f32 v38, v76, v77
	v_cvt_pk_f16_f32 v39, v78, v79
	v_pk_max_f16 v79, v39, 0
	v_pk_max_f16 v78, v38, 0
	v_pk_max_f16 v77, v37, 0
	v_pk_max_f16 v76, v36, 0
	v_cvt_pk_f16_f32 v36, v80, v81
	s_waitcnt vmcnt(0) lgkmcnt(12)
	v_mfma_f32_32x32x16_f16 v[48:63], v[40:43], v[20:23], v[48:63]
	v_cvt_pk_f16_f32 v38, v84, v85
	v_cvt_pk_f16_f32 v39, v86, v87
	ds_read_b128 v[84:87], v255 offset:5120
	v_cvt_pk_f16_f32 v37, v82, v83
	v_pk_max_f16 v80, v36, 0
	v_cvt_pk_f16_f32 v36, v92, v93
	s_mov_b32 s6, 0x20000
	s_waitcnt vmcnt(0) lgkmcnt(12)
	v_mfma_f32_32x32x16_f16 v[48:63], v[170:173], v[24:27], v[48:63]
	v_pk_max_f16 v83, v39, 0
	v_pk_max_f16 v81, v37, 0
	v_cvt_pk_f16_f32 v39, v90, v91
	v_cvt_pk_f16_f32 v37, v94, v95
	v_pk_max_f16 v90, v36, 0
	v_add_co_u32_e32 v36, vcc, s6, v156
	s_waitcnt vmcnt(0) lgkmcnt(10)
	v_mfma_f32_32x32x16_f16 v[48:63], v[166:169], v[64:67], v[48:63]
	v_pk_max_f16 v82, v38, 0
	v_pk_max_f16 v91, v37, 0
	v_addc_co_u32_e32 v37, vcc, 0, v157, vcc
	ds_read_b128 v[92:95], v255 offset:7168
	v_cvt_pk_f16_f32 v207, v44, v45
	v_and_b32_e32 v190, 0x7fff7fff, v207
	v_mfma_f32_32x32x16_f16 v[48:63], v[182:185], v[76:79], v[48:63]
	ds_read_b128 v[166:169], v255 offset:10240
	v_pk_fma_f16 v44, v190, s2, v164 op_sel_hi:[1,0,0]
	v_cvt_pk_f16_f32 v38, v88, v89
	v_pk_fma_f16 v44, v44, v190, s3 op_sel_hi:[1,1,0]
	v_pk_max_f16 v88, v38, 0
	v_pk_mul_f16 v44, v190, v44
	v_pk_add_f16 v38, v159, v153
	s_waitcnt vmcnt(0) lgkmcnt(10)
	v_mfma_f32_32x32x16_f16 v[48:63], v[116:119], v[80:83], v[48:63]
	ds_read_b128 v[116:119], v255 offset:26944
	v_exp_f16_e32 v45, v44
	v_exp_f16_sdwa v36, v44 dst_sel:DWORD dst_unused:UNUSED_PAD src0_sel:WORD_1
	v_pack_b32_f16 v37, v165, v206
	v_cvt_pk_f16_f32 v155, v46, v47
	v_pk_max_f16 v89, v39, 0
	v_pk_fma_f16 v153, v159, v37, v38 neg_lo:[1,0,0] neg_hi:[1,0,0]
	v_and_b32_e32 v159, 0x7fff7fff, v155
	s_waitcnt vmcnt(0) lgkmcnt(10)
	v_mfma_f32_32x32x16_f16 v[48:63], v[124:127], v[88:91], v[48:63]
	v_pk_fma_f16 v124, v159, s2, v164 op_sel_hi:[1,0,0]
	v_pack_b32_f16 v154, v45, v36
	v_pk_fma_f16 v124, v124, v159, s3 op_sel_hi:[1,1,0]
	v_pk_add_f16 v171, v190, v207
	v_pk_mul_f16 v165, v159, v124
	ds_read_b128 v[124:127], v255 offset:11264
	v_exp_f16_e32 v170, v165
	s_waitcnt vmcnt(0) lgkmcnt(10)
	v_mfma_f32_32x32x16_f16 v[32:47], v[32:35], v[96:99], 0
	v_exp_f16_sdwa v165, v165 dst_sel:DWORD dst_unused:UNUSED_PAD src0_sel:WORD_1
	v_pk_fma_f16 v154, v190, v154, v171 neg_lo:[1,0,0] neg_hi:[1,0,0]
	s_mov_b32 s6, 0x1e000
	v_cvt_pk_f16_f32 v4, v4, v5
	v_and_b32_e32 v5, 0x7fff7fff, v4
	v_cvt_pk_f16_f32 v56, v56, v57
	v_cvt_pk_f16_f32 v57, v58, v59
	s_waitcnt vmcnt(0) lgkmcnt(9)
	v_mfma_f32_32x32x16_f16 v[32:47], v[16:19], v[174:177], v[32:47]
	v_pack_b32_f16 v16, v170, v165
	ds_read_b128 v[170:173], v255 offset:12288
	v_add_co_u32_e32 v174, vcc, s6, v156
	v_cvt_pk_f16_f32 v18, v0, v1
	s_nop 0
	v_addc_co_u32_e32 v175, vcc, 0, v157, vcc
	s_waitcnt vmcnt(0) lgkmcnt(9)
	v_mfma_f32_32x32x16_f16 v[32:47], v[132:135], v[128:131], v[32:47]
	ds_read_b128 v[128:131], v255 offset:13312
	v_and_b32_e32 v19, 0x7fff7fff, v18
	ds_read_b128 v[132:135], v255 offset:14336
	v_pk_fma_f16 v0, v19, s2, v164 op_sel_hi:[1,0,0]
	v_pk_add_f16 v17, v159, v155
	v_pk_fma_f16 v0, v0, v19, s3 op_sel_hi:[1,1,0]
	s_mov_b32 s6, 0x1d000
	v_mfma_f32_32x32x16_f16 v[32:47], v[28:31], v[20:23], v[32:47]
	v_pk_mul_f16 v0, v19, v0
	v_pk_fma_f16 v155, v159, v16, v17 neg_lo:[1,0,0] neg_hi:[1,0,0]
	v_exp_f16_e32 v1, v0
	v_exp_f16_sdwa v0, v0 dst_sel:DWORD dst_unused:UNUSED_PAD src0_sel:WORD_1
	v_add_co_u32_e32 v16, vcc, s6, v156
	v_cvt_pk_f16_f32 v20, v2, v3
	s_nop 0
	v_addc_co_u32_e32 v17, vcc, 0, v157, vcc
	v_pack_b32_f16 v159, v1, v0
	s_waitcnt vmcnt(0) lgkmcnt(10)
	v_mfma_f32_32x32x16_f16 v[32:47], v[68:71], v[24:27], v[32:47]
	ds_read_b128 v[0:3], v255 offset:15360
	v_and_b32_e32 v21, 0x7fff7fff, v20
	v_pk_fma_f16 v22, v21, s2, v164 op_sel_hi:[1,0,0]
	v_pk_add_f16 v18, v19, v18
	v_pk_fma_f16 v22, v22, v21, s3 op_sel_hi:[1,1,0]
	v_pk_fma_f16 v68, v19, v159, v18 neg_lo:[1,0,0] neg_hi:[1,0,0]
	v_pk_mul_f16 v22, v21, v22
	s_waitcnt vmcnt(0) lgkmcnt(10)
	v_mfma_f32_32x32x16_f16 v[32:47], v[72:75], v[64:67], v[32:47]
	ds_read_b128 v[64:67], v255 offset:16384
	ds_read_b128 v[72:75], v255 offset:17728
	v_pk_fma_f16 v16, v5, s2, v164 op_sel_hi:[1,0,0]
	v_cvt_pk_f16_f32 v17, v50, v51
	v_pk_fma_f16 v70, v16, v5, s3 op_sel_hi:[1,1,0]
	v_cvt_pk_f16_f32 v16, v48, v49
	ds_read_b128 v[48:51], v255 offset:18752
	s_waitcnt vmcnt(0) lgkmcnt(12)
	v_mfma_f32_32x32x16_f16 v[32:47], v[160:163], v[76:79], v[32:47]
	v_exp_f16_e32 v23, v22
	v_exp_f16_sdwa v22, v22 dst_sel:DWORD dst_unused:UNUSED_PAD src0_sel:WORD_1
	ds_read_b128 v[76:79], v255 offset:19776
	v_pk_add_f16 v19, v21, v20
	v_cvt_pk_f16_f32 v58, v60, v61
	v_pack_b32_f16 v18, v23, v22
	v_pk_fma_f16 v69, v21, v18, v19 neg_lo:[1,0,0] neg_hi:[1,0,0]
	s_waitcnt vmcnt(0) lgkmcnt(12)
	v_mfma_f32_32x32x16_f16 v[32:47], v[84:87], v[80:83], v[32:47]
	v_cvt_pk_f16_f32 v18, v52, v53
	v_cvt_pk_f16_f32 v19, v54, v55
	v_pk_max_f16 v55, v19, 0
	v_pk_max_f16 v54, v18, 0
	v_pk_max_f16 v53, v17, 0
	v_pk_max_f16 v52, v16, 0
	v_cvt_pk_f16_f32 v59, v62, v63
	s_waitcnt vmcnt(0) lgkmcnt(9)
	v_mfma_f32_32x32x16_f16 v[16:31], v[116:119], v[96:99], 0
	ds_read_b128 v[60:63], v255 offset:20800
	v_pk_max_f16 v59, v59, 0
	v_pk_max_f16 v58, v58, 0
	v_pk_max_f16 v57, v57, 0
	v_pk_max_f16 v56, v56, 0
	v_cvt_pk_f16_f32 v6, v6, v7
	v_and_b32_e32 v7, 0x7fff7fff, v6
	v_mfma_f32_32x32x16_f16 v[32:47], v[92:95], v[88:91], v[32:47]
	v_pk_add_f16 v4, v5, v4
	s_mov_b32 s6, 0x1f000
	v_mfma_f32_32x32x16_f16 v[16:31], v[166:169], v[52:55], v[16:31]
	s_nop 8
	v_cvt_pk_f16_f32 v32, v32, v33
	v_cvt_pk_f16_f32 v33, v34, v35
	v_cvt_pk_f16_f32 v34, v36, v37
	v_cvt_pk_f16_f32 v35, v38, v39
	ds_read_b128 v[36:39], v255 offset:21824
	v_pk_max_f16 v35, v35, 0
	v_pk_max_f16 v34, v34, 0
	s_waitcnt vmcnt(0) lgkmcnt(10)
	v_mfma_f32_32x32x16_f16 v[16:31], v[124:127], v[56:59], v[16:31]
	v_pk_max_f16 v33, v33, 0
	v_pk_max_f16 v32, v32, 0
	v_cvt_pk_f16_f32 v40, v40, v41
	v_add_co_u32_e32 v56, vcc, s6, v156
	s_nop 1
	v_addc_co_u32_e32 v57, vcc, 0, v157, vcc
	s_waitcnt vmcnt(0) lgkmcnt(9)
	v_mfma_f32_32x32x16_f16 v[16:31], v[170:173], v[32:35], v[16:31]
	v_cvt_pk_f16_f32 v32, v42, v43
	v_cvt_pk_f16_f32 v33, v44, v45
	v_cvt_pk_f16_f32 v34, v46, v47
	v_pk_max_f16 v35, v34, 0
	v_pk_max_f16 v34, v33, 0
	v_pk_max_f16 v33, v32, 0
	v_pk_max_f16 v32, v40, 0
	ds_read_b128 v[52:55], v255 offset:22848
	s_waitcnt vmcnt(0) lgkmcnt(9)
	v_mfma_f32_32x32x16_f16 v[16:31], v[128:131], v[32:35], v[16:31]
	v_pk_fma_f16 v34, v7, s2, v164 op_sel_hi:[1,0,0]
	v_pk_mul_f16 v32, v5, v70
	v_pk_fma_f16 v34, v34, v7, s3 op_sel_hi:[1,1,0]
	v_exp_f16_e32 v33, v32
	v_exp_f16_sdwa v32, v32 dst_sel:DWORD dst_unused:UNUSED_PAD src0_sel:WORD_1
	v_pk_mul_f16 v34, v7, v34
	v_pack_b32_f16 v32, v33, v32
	s_waitcnt vmcnt(0) lgkmcnt(8)
	v_mfma_f32_32x32x16_f16 v[16:31], v[132:135], v[120:123], v[16:31]
	v_exp_f16_e32 v35, v34
	v_exp_f16_sdwa v34, v34 dst_sel:DWORD dst_unused:UNUSED_PAD src0_sel:WORD_1
	v_pk_fma_f16 v70, v5, v32, v4 neg_lo:[1,0,0] neg_hi:[1,0,0]
	v_pack_b32_f16 v4, v35, v34
	s_waitcnt vmcnt(0) lgkmcnt(7)
	v_mfma_f32_32x32x16_f16 v[16:31], v[0:3], v[136:139], v[16:31]
	v_pk_add_f16 v0, v7, v6
	s_nop 0
	v_pk_fma_f16 v71, v7, v4, v0 neg_lo:[1,0,0] neg_hi:[1,0,0]
	v_cvt_pk_f16_f32 v0, v8, v9
	v_and_b32_e32 v1, 0x7fff7fff, v0
	v_cvt_pk_f16_f32 v4, v10, v11
	v_pk_fma_f16 v2, v1, s2, v164 op_sel_hi:[1,0,0]
	s_waitcnt vmcnt(0) lgkmcnt(6)
	v_mfma_f32_32x32x16_f16 v[16:31], v[64:67], v[140:143], v[16:31]
	v_and_b32_e32 v5, 0x7fff7fff, v4
	v_pk_fma_f16 v2, v2, v1, s3 op_sel_hi:[1,1,0]
	v_pk_fma_f16 v6, v5, s2, v164 op_sel_hi:[1,0,0]
	v_pk_mul_f16 v2, v1, v2
	v_pk_fma_f16 v6, v6, v5, s3 op_sel_hi:[1,1,0]
	v_exp_f16_e32 v3, v2
	v_exp_f16_sdwa v2, v2 dst_sel:DWORD dst_unused:UNUSED_PAD src0_sel:WORD_1
	s_waitcnt vmcnt(0) lgkmcnt(5)
	v_mfma_f32_32x32x16_f16 v[16:31], v[72:75], v[144:147], v[16:31]
	v_pk_mul_f16 v6, v5, v6
	v_pk_add_f16 v0, v1, v0
	v_exp_f16_e32 v7, v6
	v_exp_f16_sdwa v6, v6 dst_sel:DWORD dst_unused:UNUSED_PAD src0_sel:WORD_1
	v_pack_b32_f16 v2, v3, v2
	v_pk_fma_f16 v0, v1, v2, v0 neg_lo:[1,0,0] neg_hi:[1,0,0]
	v_pk_add_f16 v2, v5, v4
	s_waitcnt vmcnt(0) lgkmcnt(4)
	v_mfma_f32_32x32x16_f16 v[16:31], v[48:51], v[148:151], v[16:31]
	v_pack_b32_f16 v1, v7, v6
	v_pk_fma_f16 v1, v5, v1, v2 neg_lo:[1,0,0] neg_hi:[1,0,0]
	v_cvt_pk_f16_f32 v2, v12, v13
	v_and_b32_e32 v3, 0x7fff7fff, v2
	v_cvt_pk_f16_f32 v6, v14, v15
	v_pk_fma_f16 v4, v3, s2, v164 op_sel_hi:[1,0,0]
	v_and_b32_e32 v7, 0x7fff7fff, v6
	s_waitcnt vmcnt(0) lgkmcnt(3)
	v_mfma_f32_32x32x16_f16 v[16:31], v[76:79], v[152:155], v[16:31]
	v_pk_fma_f16 v4, v4, v3, s3 op_sel_hi:[1,1,0]
	v_pk_fma_f16 v8, v7, s2, v164 op_sel_hi:[1,0,0]
	v_pk_mul_f16 v4, v3, v4
	v_pk_fma_f16 v8, v8, v7, s3 op_sel_hi:[1,1,0]
	v_exp_f16_e32 v5, v4
	v_exp_f16_sdwa v4, v4 dst_sel:DWORD dst_unused:UNUSED_PAD src0_sel:WORD_1
	v_pk_mul_f16 v8, v7, v8
	s_waitcnt vmcnt(0) lgkmcnt(2)
	v_mfma_f32_32x32x16_f16 v[16:31], v[60:63], v[68:71], v[16:31]
	v_exp_f16_e32 v9, v8
	v_exp_f16_sdwa v8, v8 dst_sel:DWORD dst_unused:UNUSED_PAD src0_sel:WORD_1
	v_pack_b32_f16 v4, v5, v4
	v_pk_add_f16 v2, v3, v2
	s_nop 0
	v_pk_fma_f16 v2, v3, v4, v2 neg_lo:[1,0,0] neg_hi:[1,0,0]
	v_pack_b32_f16 v3, v9, v8
	v_pk_add_f16 v4, v7, v6
	s_nop 0
	v_pk_fma_f16 v3, v7, v3, v4 neg_lo:[1,0,0] neg_hi:[1,0,0]
	ds_read_b128 v[4:7], v255 offset:24896
	s_waitcnt vmcnt(0) lgkmcnt(2)
	v_mfma_f32_32x32x16_f16 v[16:31], v[36:39], v[0:3], v[16:31]
	ds_read_b128 v[0:3], v255 offset:23872
	s_waitcnt vmcnt(0) lgkmcnt(2)
	v_mfma_f32_32x32x16_f16 v[16:31], v[52:55], v[104:107], v[16:31]
	s_waitcnt vmcnt(0) lgkmcnt(0)
	v_mfma_f32_32x32x16_f16 v[16:31], v[0:3], v[100:103], v[16:31]
	ds_read_b128 v[0:3], v255 offset:25920
	v_mfma_f32_32x32x16_f16 v[16:31], v[4:7], v[112:115], v[16:31]
	s_waitcnt vmcnt(0) lgkmcnt(0)
	v_mfma_f32_32x32x16_f16 v[16:31], v[0:3], v[108:111], v[16:31]
	s_nop 11
	ds_bpermute_b32 v3, v209, v16
	ds_bpermute_b32 v2, v209, v17
	ds_bpermute_b32 v1, v209, v18
	ds_bpermute_b32 v0, v209, v19
	s_and_saveexec_b64 s[2:3], s[0:1]
	s_cbranch_execz .LBB0_33
	v_max_f32_e32 v4, v17, v17
	v_max_f32_e32 v5, v16, v16
	v_max_f32_e32 v4, v5, v4
	v_max_f32_e32 v5, v19, v19
	v_max_f32_e32 v6, v18, v18
	v_max_f32_e32 v5, v6, v5
	s_waitcnt vmcnt(0) lgkmcnt(3)
	v_max3_f32 v6, v4, v5, v3
	v_sub_f32_e32 v4, v16, v6
	v_sub_f32_e32 v5, v17, v6
	v_sub_f32_e32 v7, v18, v6
	v_mul_f32_e32 v4, 0x3fb8aa3b, v4
	v_mul_f32_e32 v5, 0x3fb8aa3b, v5
	v_mul_f32_e32 v7, 0x3fb8aa3b, v7
	v_exp_f32_e32 v4, v4
	v_exp_f32_e32 v5, v5
	v_exp_f32_e32 v9, v7
	v_sub_f32_e32 v7, v19, v6
	v_mul_f32_e32 v7, 0x3fb8aa3b, v7
	v_sub_f32_e32 v6, v3, v6
	v_exp_f32_e32 v7, v7
	v_mul_f32_e32 v6, 0x3fb8aa3b, v6
	v_exp_f32_e32 v6, v6
	v_add_f32_e32 v8, v4, v5
	v_add_f32_e32 v8, v9, v8
	v_add_f32_e32 v8, v7, v8
	v_add_f32_e32 v8, v6, v8
	v_rcp_f32_e32 v8, v8
	s_waitcnt vmcnt(0) lgkmcnt(1)
	v_mul_f32_e32 v1, 0xbfb8aa3b, v1
	v_exp_f32_e32 v1, v1
	s_mov_b32 s1, 0x403fba14
	v_pk_mul_f32 v[6:7], v[6:7], v[8:9] op_sel_hi:[1,0]
	s_mov_b32 s0, 0x40f33a98
	v_pk_mul_f32 v[20:21], v[4:5], v[8:9] op_sel_hi:[1,0]
	v_pk_mul_f32 v[14:15], v[6:7], s[0:1]
	s_mov_b32 s0, 0x411e74af
	v_add_f32_e32 v4, v20, v21
	v_mul_f32_e32 v12, v9, v8
	v_fmac_f32_e32 v4, v9, v8
	v_pk_mul_f32 v[8:9], v[20:21], s[0:1]
	s_mov_b32 s3, 0x4108466c
	s_mov_b32 s2, s1
	v_add_f32_e32 v1, 1.0, v1
	v_mul_f32_e32 v13, 0x411e74af, v6
	v_pk_fma_f32 v[8:9], v[20:21], s[2:3], v[8:9] op_sel:[0,0,1] op_sel_hi:[1,1,0]
	s_mov_b32 s2, 0x40dd0c55
	s_mov_b32 s3, s0
	v_max_f32_e32 v2, v2, v2
	v_rcp_f32_e32 v1, v1
	v_mul_f32_e32 v7, 0x40c6de12, v7
	v_pk_fma_f32 v[8:9], v[12:13], s[2:3], v[8:9] op_sel_hi:[0,1,1]
	v_mov_b32_e32 v6, v15
	v_max_f32_e32 v2, 0xc1400000, v2
	v_pk_add_f32 v[6:7], v[6:7], v[8:9]
	v_mov_b32_e32 v15, v13
	v_min_f32_e32 v2, 0x41400000, v2
	v_pk_add_f32 v[6:7], v[14:15], v[6:7]
	s_mov_b32 s4, 0xbfb8aa3b
	v_mul_f32_e32 v4, v2, v4
	v_sub_f32_e32 v2, v7, v6
	v_fmac_f32_e32 v6, v1, v2
	s_waitcnt vmcnt(0) lgkmcnt(0)
	v_mul_f32_e64 v1, |v0|, s4
	v_exp_f32_e32 v1, v1
	v_max_f32_e32 v0, v0, v0
	v_mov_b32_e32 v2, 0x411e74af
	v_max_f32_e32 v0, 0, v0
	v_add_f32_e32 v1, 1.0, v1
	v_log_f32_e32 v1, v1
	v_med3_f32 v2, v6, s1, v2
	v_mul_f32_e32 v2, 0x3fb8aa3b, v2
	v_exp_f32_e32 v5, v2
	v_fmamk_f32 v0, v1, 0x3f317218, v0
	v_add_f32_e32 v0, 0x3dcccccd, v0
	v_max_f32_e32 v0, 0x3dcccccd, v0
	v_min_f32_e32 v6, 0x41200000, v0
	v_lshlrev_b32_e32 v0, 3, v158
	v_mov_b32_e32 v10, s38
	v_mov_b32_e32 v11, s39
	v_ashrrev_i32_e32 v1, 31, v0
	v_lshl_add_u64 v[8:9], v[0:1], 2, v[10:11]
	v_mov_b32_e32 v7, v16
	v_pk_mov_b32 v[0:1], v[16:17], v[18:19] op_sel:[1,0]
	v_mov_b32_e32 v2, v19
	global_store_dwordx4 v[8:9], v[4:7], off
	global_store_dwordx4 v[8:9], v[0:3], off offset:16
